# v8s+meta + GEMM K-loops: the barrier ahead of each 32-MFMA block moved behind its first 4 MFMAs (operands already in registers) so the matrix pipe has work during the barrier release
# speedup vs baseline: 1.0025x; 1.0012x over previous
.LBB0_148:
	ds_read_b128 v[154:157], v172
	ds_read_b128 v[158:161], v172 offset:1024
	ds_read_b128 v[162:165], v172 offset:2048
	ds_read_b128 v[180:183], v172 offset:3072
	ds_read_b128 v[184:187], v173
	ds_read_b128 v[188:191], v173 offset:1024
	ds_read_b128 v[192:195], v173 offset:2048
	ds_read_b128 v[196:199], v173 offset:3072
	s_add_u32 s26, s24, 0xfff80080
	s_addc_u32 s27, s25, -1
	s_cmp_eq_u32 s36, 28
	s_cselect_b32 s29, s3, s27
	s_cselect_b32 s28, s7, s26
	s_cselect_b32 s27, s8, s33
	s_cselect_b32 s26, s17, s19
	v_lshl_add_u64 v[232:233], s[24:25], 0, v[146:147]
	s_add_i32 m0, s35, 0xc000
	ds_read_b128 v[200:203], v174
	ds_read_b128 v[204:207], v174 offset:1024
	ds_read_b128 v[208:211], v174 offset:2048
	ds_read_b128 v[212:215], v174 offset:3072
	ds_read_b128 v[216:219], v174 offset:4096
	ds_read_b128 v[220:223], v174 offset:5120
	ds_read_b128 v[224:227], v174 offset:6144
	ds_read_b128 v[228:231], v174 offset:7168
	global_load_lds_dwordx4 v[232:233], off
	v_lshl_add_u64 v[232:233], s[24:25], 0, v[148:149]
	s_add_i32 m0, s35, 0xe000
	s_nop 0
	global_load_lds_dwordx4 v[232:233], off
	s_waitcnt vmcnt(8)
	s_waitcnt lgkmcnt(0)
	s_setprio 1
	s_waitcnt lgkmcnt(0)
	v_mfma_f32_16x16x32_bf16 v[124:127], v[154:157], v[200:203], v[124:127]
	v_mfma_f32_16x16x32_bf16 v[116:119], v[162:165], v[200:203], v[116:119]
	v_mfma_f32_16x16x32_bf16 v[108:111], v[154:157], v[208:211], v[108:111]
	v_mfma_f32_16x16x32_bf16 v[100:103], v[162:165], v[208:211], v[100:103]
	s_barrier
	v_mfma_f32_16x16x32_bf16 v[92:95], v[154:157], v[216:219], v[92:95]
	v_mfma_f32_16x16x32_bf16 v[84:87], v[162:165], v[216:219], v[84:87]
	v_mfma_f32_16x16x32_bf16 v[76:79], v[154:157], v[224:227], v[76:79]
	v_mfma_f32_16x16x32_bf16 v[68:71], v[162:165], v[224:227], v[68:71]
	v_mfma_f32_16x16x32_bf16 v[124:127], v[158:161], v[204:207], v[124:127]
	v_mfma_f32_16x16x32_bf16 v[116:119], v[180:183], v[204:207], v[116:119]
	v_mfma_f32_16x16x32_bf16 v[108:111], v[158:161], v[212:215], v[108:111]
	v_mfma_f32_16x16x32_bf16 v[100:103], v[180:183], v[212:215], v[100:103]
	v_mfma_f32_16x16x32_bf16 v[92:95], v[158:161], v[220:223], v[92:95]
	v_mfma_f32_16x16x32_bf16 v[84:87], v[180:183], v[220:223], v[84:87]
	v_mfma_f32_16x16x32_bf16 v[76:79], v[158:161], v[228:231], v[76:79]
	v_mfma_f32_16x16x32_bf16 v[68:71], v[180:183], v[228:231], v[68:71]
	s_setprio 0
	s_setprio 1
	v_mfma_f32_16x16x32_bf16 v[120:123], v[184:187], v[200:203], v[120:123]
	v_mfma_f32_16x16x32_bf16 v[112:115], v[192:195], v[200:203], v[112:115]
	v_mfma_f32_16x16x32_bf16 v[104:107], v[184:187], v[208:211], v[104:107]
	v_mfma_f32_16x16x32_bf16 v[96:99], v[192:195], v[208:211], v[96:99]
	v_mfma_f32_16x16x32_bf16 v[88:91], v[184:187], v[216:219], v[88:91]
	v_mfma_f32_16x16x32_bf16 v[80:83], v[192:195], v[216:219], v[80:83]
	v_mfma_f32_16x16x32_bf16 v[72:75], v[184:187], v[224:227], v[72:75]
	v_mfma_f32_16x16x32_bf16 v[64:67], v[192:195], v[224:227], v[64:67]
	v_mfma_f32_16x16x32_bf16 v[120:123], v[188:191], v[204:207], v[120:123]
	v_mfma_f32_16x16x32_bf16 v[112:115], v[196:199], v[204:207], v[112:115]
	v_mfma_f32_16x16x32_bf16 v[104:107], v[188:191], v[212:215], v[104:107]
	v_mfma_f32_16x16x32_bf16 v[96:99], v[196:199], v[212:215], v[96:99]
	v_mfma_f32_16x16x32_bf16 v[88:91], v[188:191], v[220:223], v[88:91]
	v_mfma_f32_16x16x32_bf16 v[80:83], v[196:199], v[220:223], v[80:83]
	v_mfma_f32_16x16x32_bf16 v[72:75], v[188:191], v[228:231], v[72:75]
	v_mfma_f32_16x16x32_bf16 v[64:67], v[196:199], v[228:231], v[64:67]
	s_setprio 0
	s_barrier
	s_add_i32 s37, s79, s34
	v_lshl_add_u64 v[232:233], s[26:27], 0, v[130:131]
	s_mov_b32 m0, s37
	ds_read_b128 v[200:203], v174 offset:16384
	ds_read_b128 v[204:207], v174 offset:17408
	ds_read_b128 v[208:211], v174 offset:18432
	ds_read_b128 v[212:215], v174 offset:19456
	ds_read_b128 v[216:219], v174 offset:20480
	ds_read_b128 v[220:223], v174 offset:21504
	ds_read_b128 v[224:227], v174 offset:22528
	ds_read_b128 v[228:231], v174 offset:23552
	global_load_lds_dwordx4 v[232:233], off
	s_add_i32 m0, s37, 0x2000
	s_add_u32 s38, s26, 0x80000
	v_lshl_add_u64 v[234:235], s[26:27], 0, v[134:135]
	s_addc_u32 s39, s27, 0
	s_add_i32 s37, s81, s34
	global_load_lds_dwordx4 v[234:235], off
	v_lshl_add_u64 v[236:237], s[38:39], 0, v[130:131]
	s_mov_b32 m0, s37
	v_lshl_add_u64 v[238:239], s[28:29], 0, v[132:133]
	global_load_lds_dwordx4 v[236:237], off
	v_lshl_add_u64 v[236:237], s[38:39], 0, v[134:135]
	s_add_i32 m0, s37, 0x2000
	s_nop 0
	global_load_lds_dwordx4 v[236:237], off
	v_lshl_add_u64 v[236:237], s[28:29], 0, v[128:129]
	s_mov_b32 m0, s35
	s_nop 0
	global_load_lds_dwordx4 v[236:237], off
	s_mov_b32 m0, s54
	s_nop 0
	global_load_lds_dwordx4 v[238:239], off
	s_waitcnt vmcnt(8)
	s_waitcnt lgkmcnt(0)
	s_setprio 1
	s_waitcnt lgkmcnt(0)
	v_mfma_f32_16x16x32_bf16 v[60:63], v[154:157], v[200:203], v[60:63]
	v_mfma_f32_16x16x32_bf16 v[52:55], v[162:165], v[200:203], v[52:55]
	v_mfma_f32_16x16x32_bf16 v[44:47], v[154:157], v[208:211], v[44:47]
	v_mfma_f32_16x16x32_bf16 v[36:39], v[162:165], v[208:211], v[36:39]
	s_barrier
	v_mfma_f32_16x16x32_bf16 v[28:31], v[154:157], v[216:219], v[28:31]
	v_mfma_f32_16x16x32_bf16 v[20:23], v[162:165], v[216:219], v[20:23]
	v_mfma_f32_16x16x32_bf16 v[12:15], v[154:157], v[224:227], v[12:15]
	v_mfma_f32_16x16x32_bf16 v[4:7], v[162:165], v[224:227], v[4:7]
	v_mfma_f32_16x16x32_bf16 v[60:63], v[158:161], v[204:207], v[60:63]
	v_mfma_f32_16x16x32_bf16 v[52:55], v[180:183], v[204:207], v[52:55]
	v_mfma_f32_16x16x32_bf16 v[44:47], v[158:161], v[212:215], v[44:47]
	v_mfma_f32_16x16x32_bf16 v[36:39], v[180:183], v[212:215], v[36:39]
	v_mfma_f32_16x16x32_bf16 v[28:31], v[158:161], v[220:223], v[28:31]
	v_mfma_f32_16x16x32_bf16 v[20:23], v[180:183], v[220:223], v[20:23]
	v_mfma_f32_16x16x32_bf16 v[12:15], v[158:161], v[228:231], v[12:15]
	v_mfma_f32_16x16x32_bf16 v[4:7], v[180:183], v[228:231], v[4:7]
	s_setprio 0
	s_setprio 1
	v_mfma_f32_16x16x32_bf16 v[56:59], v[184:187], v[200:203], v[56:59]
	v_mfma_f32_16x16x32_bf16 v[48:51], v[192:195], v[200:203], v[48:51]
	v_mfma_f32_16x16x32_bf16 v[40:43], v[184:187], v[208:211], v[40:43]
	v_mfma_f32_16x16x32_bf16 v[32:35], v[192:195], v[208:211], v[32:35]
	v_mfma_f32_16x16x32_bf16 v[24:27], v[184:187], v[216:219], v[24:27]
	v_mfma_f32_16x16x32_bf16 v[16:19], v[192:195], v[216:219], v[16:19]
	v_mfma_f32_16x16x32_bf16 v[8:11], v[184:187], v[224:227], v[8:11]
	v_mfma_f32_16x16x32_bf16 v[0:3], v[192:195], v[224:227], v[0:3]
	v_mfma_f32_16x16x32_bf16 v[56:59], v[188:191], v[204:207], v[56:59]
	v_mfma_f32_16x16x32_bf16 v[48:51], v[196:199], v[204:207], v[48:51]
	v_mfma_f32_16x16x32_bf16 v[40:43], v[188:191], v[212:215], v[40:43]
	v_mfma_f32_16x16x32_bf16 v[32:35], v[196:199], v[212:215], v[32:35]
	v_mfma_f32_16x16x32_bf16 v[24:27], v[188:191], v[220:223], v[24:27]
	v_mfma_f32_16x16x32_bf16 v[16:19], v[196:199], v[220:223], v[16:19]
	v_mfma_f32_16x16x32_bf16 v[8:11], v[188:191], v[228:231], v[8:11]
	v_mfma_f32_16x16x32_bf16 v[0:3], v[196:199], v[228:231], v[0:3]
	s_setprio 0
	s_barrier
	s_add_i32 s37, 0, 0x18000
	v_add_u32_e32 v136, s37, v141
	s_add_i32 s38, 0, 0x1c000
	ds_read_b128 v[154:157], v136
	ds_read_b128 v[158:161], v136 offset:1024
	ds_read_b128 v[162:165], v136 offset:2048
	ds_read_b128 v[180:183], v136 offset:3072
	v_add_u32_e32 v136, s38, v141
	ds_read_b128 v[184:187], v136
	ds_read_b128 v[188:191], v136 offset:1024
	ds_read_b128 v[192:195], v136 offset:2048
	ds_read_b128 v[196:199], v136 offset:3072
	s_add_u32 s28, s28, 0x80000
	s_addc_u32 s29, s29, 0
	s_mov_b32 m0, s55
	v_lshl_add_u64 v[240:241], s[28:29], 0, v[128:129]
	ds_read_b128 v[200:203], v174 offset:32768
	ds_read_b128 v[204:207], v174 offset:33792
	ds_read_b128 v[208:211], v174 offset:34816
	ds_read_b128 v[212:215], v174 offset:35840
	ds_read_b128 v[216:219], v174 offset:36864
	ds_read_b128 v[220:223], v174 offset:37888
	ds_read_b128 v[224:227], v174 offset:38912
	ds_read_b128 v[228:231], v174 offset:39936
	global_load_lds_dwordx4 v[240:241], off
	v_lshl_add_u64 v[240:241], s[28:29], 0, v[132:133]
	s_mov_b32 m0, s56
	s_nop 0
	global_load_lds_dwordx4 v[240:241], off
	s_waitcnt vmcnt(8)
	s_waitcnt lgkmcnt(0)
	s_setprio 1
	s_waitcnt lgkmcnt(0)
	v_mfma_f32_16x16x32_bf16 v[124:127], v[154:157], v[200:203], v[124:127]
	v_mfma_f32_16x16x32_bf16 v[116:119], v[162:165], v[200:203], v[116:119]
	v_mfma_f32_16x16x32_bf16 v[108:111], v[154:157], v[208:211], v[108:111]
	v_mfma_f32_16x16x32_bf16 v[100:103], v[162:165], v[208:211], v[100:103]
	s_barrier
	v_mfma_f32_16x16x32_bf16 v[92:95], v[154:157], v[216:219], v[92:95]
	v_mfma_f32_16x16x32_bf16 v[84:87], v[162:165], v[216:219], v[84:87]
	v_mfma_f32_16x16x32_bf16 v[76:79], v[154:157], v[224:227], v[76:79]
	v_mfma_f32_16x16x32_bf16 v[68:71], v[162:165], v[224:227], v[68:71]
	v_mfma_f32_16x16x32_bf16 v[124:127], v[158:161], v[204:207], v[124:127]
	v_mfma_f32_16x16x32_bf16 v[116:119], v[180:183], v[204:207], v[116:119]
	v_mfma_f32_16x16x32_bf16 v[108:111], v[158:161], v[212:215], v[108:111]
	v_mfma_f32_16x16x32_bf16 v[100:103], v[180:183], v[212:215], v[100:103]
	v_mfma_f32_16x16x32_bf16 v[92:95], v[158:161], v[220:223], v[92:95]
	v_mfma_f32_16x16x32_bf16 v[84:87], v[180:183], v[220:223], v[84:87]
	v_mfma_f32_16x16x32_bf16 v[76:79], v[158:161], v[228:231], v[76:79]
	v_mfma_f32_16x16x32_bf16 v[68:71], v[180:183], v[228:231], v[68:71]
	s_setprio 0
	s_setprio 1
	v_mfma_f32_16x16x32_bf16 v[120:123], v[184:187], v[200:203], v[120:123]
	v_mfma_f32_16x16x32_bf16 v[112:115], v[192:195], v[200:203], v[112:115]
	v_mfma_f32_16x16x32_bf16 v[104:107], v[184:187], v[208:211], v[104:107]
	v_mfma_f32_16x16x32_bf16 v[96:99], v[192:195], v[208:211], v[96:99]
	v_mfma_f32_16x16x32_bf16 v[88:91], v[184:187], v[216:219], v[88:91]
	v_mfma_f32_16x16x32_bf16 v[80:83], v[192:195], v[216:219], v[80:83]
	v_mfma_f32_16x16x32_bf16 v[72:75], v[184:187], v[224:227], v[72:75]
	v_mfma_f32_16x16x32_bf16 v[64:67], v[192:195], v[224:227], v[64:67]
	v_mfma_f32_16x16x32_bf16 v[120:123], v[188:191], v[204:207], v[120:123]
	v_mfma_f32_16x16x32_bf16 v[112:115], v[196:199], v[204:207], v[112:115]
	v_mfma_f32_16x16x32_bf16 v[104:107], v[188:191], v[212:215], v[104:107]
	v_mfma_f32_16x16x32_bf16 v[96:99], v[196:199], v[212:215], v[96:99]
	v_mfma_f32_16x16x32_bf16 v[88:91], v[188:191], v[220:223], v[88:91]
	v_mfma_f32_16x16x32_bf16 v[80:83], v[196:199], v[220:223], v[80:83]
	v_mfma_f32_16x16x32_bf16 v[72:75], v[188:191], v[228:231], v[72:75]
	v_mfma_f32_16x16x32_bf16 v[64:67], v[196:199], v[228:231], v[64:67]
	s_setprio 0
	s_barrier
	s_add_i32 s28, s37, s34
	v_lshl_add_u64 v[232:233], v[232:233], 0, s[12:13]
	s_mov_b32 m0, s28
	ds_read_b128 v[200:203], v174 offset:49152
	ds_read_b128 v[204:207], v174 offset:50176
	ds_read_b128 v[208:211], v174 offset:51200
	ds_read_b128 v[212:215], v174 offset:52224
	ds_read_b128 v[216:219], v174 offset:53248
	ds_read_b128 v[220:223], v174 offset:54272
	ds_read_b128 v[224:227], v174 offset:55296
	ds_read_b128 v[228:231], v174 offset:56320
	global_load_lds_dwordx4 v[232:233], off
	s_add_i32 m0, s28, 0x2000
	s_add_u32 s26, s26, 0x80080
	v_lshl_add_u64 v[232:233], v[234:235], 0, s[12:13]
	s_addc_u32 s27, s27, 0
	s_add_i32 s28, s38, s34
	global_load_lds_dwordx4 v[232:233], off
	v_lshl_add_u64 v[232:233], s[26:27], 0, v[130:131]
	s_mov_b32 m0, s28
	s_nop 0
	global_load_lds_dwordx4 v[232:233], off
	v_lshl_add_u64 v[232:233], s[26:27], 0, v[134:135]
	s_add_i32 m0, s28, 0x2000
	s_nop 0
	global_load_lds_dwordx4 v[232:233], off
	v_lshl_add_u64 v[232:233], v[236:237], 0, s[12:13]
	s_mov_b32 m0, s62
	s_nop 0
	global_load_lds_dwordx4 v[232:233], off
	v_lshl_add_u64 v[232:233], v[238:239], 0, s[12:13]
	s_mov_b32 m0, s63
	s_nop 0
	global_load_lds_dwordx4 v[232:233], off
	s_waitcnt vmcnt(8)
	s_waitcnt lgkmcnt(0)
	s_setprio 1
	s_waitcnt lgkmcnt(0)
	v_mfma_f32_16x16x32_bf16 v[60:63], v[154:157], v[200:203], v[60:63]
	v_mfma_f32_16x16x32_bf16 v[52:55], v[162:165], v[200:203], v[52:55]
	v_mfma_f32_16x16x32_bf16 v[44:47], v[154:157], v[208:211], v[44:47]
	v_mfma_f32_16x16x32_bf16 v[36:39], v[162:165], v[208:211], v[36:39]
	s_barrier
	v_mfma_f32_16x16x32_bf16 v[28:31], v[154:157], v[216:219], v[28:31]
	v_mfma_f32_16x16x32_bf16 v[20:23], v[162:165], v[216:219], v[20:23]
	v_mfma_f32_16x16x32_bf16 v[12:15], v[154:157], v[224:227], v[12:15]
	v_mfma_f32_16x16x32_bf16 v[4:7], v[162:165], v[224:227], v[4:7]
	v_mfma_f32_16x16x32_bf16 v[60:63], v[158:161], v[204:207], v[60:63]
	v_mfma_f32_16x16x32_bf16 v[52:55], v[180:183], v[204:207], v[52:55]
	v_mfma_f32_16x16x32_bf16 v[44:47], v[158:161], v[212:215], v[44:47]
	v_mfma_f32_16x16x32_bf16 v[36:39], v[180:183], v[212:215], v[36:39]
	v_mfma_f32_16x16x32_bf16 v[28:31], v[158:161], v[220:223], v[28:31]
	v_mfma_f32_16x16x32_bf16 v[20:23], v[180:183], v[220:223], v[20:23]
	v_mfma_f32_16x16x32_bf16 v[12:15], v[158:161], v[228:231], v[12:15]
	v_mfma_f32_16x16x32_bf16 v[4:7], v[180:183], v[228:231], v[4:7]
	s_setprio 0
	s_setprio 1
	v_mfma_f32_16x16x32_bf16 v[56:59], v[184:187], v[200:203], v[56:59]
	v_mfma_f32_16x16x32_bf16 v[48:51], v[192:195], v[200:203], v[48:51]
	v_mfma_f32_16x16x32_bf16 v[40:43], v[184:187], v[208:211], v[40:43]
	v_mfma_f32_16x16x32_bf16 v[32:35], v[192:195], v[208:211], v[32:35]
	v_mfma_f32_16x16x32_bf16 v[24:27], v[184:187], v[216:219], v[24:27]
	v_mfma_f32_16x16x32_bf16 v[16:19], v[192:195], v[216:219], v[16:19]
	v_mfma_f32_16x16x32_bf16 v[8:11], v[184:187], v[224:227], v[8:11]
	v_mfma_f32_16x16x32_bf16 v[0:3], v[192:195], v[224:227], v[0:3]
	v_mfma_f32_16x16x32_bf16 v[56:59], v[188:191], v[204:207], v[56:59]
	v_mfma_f32_16x16x32_bf16 v[48:51], v[196:199], v[204:207], v[48:51]
	v_mfma_f32_16x16x32_bf16 v[40:43], v[188:191], v[212:215], v[40:43]
	v_mfma_f32_16x16x32_bf16 v[32:35], v[196:199], v[212:215], v[32:35]
	v_mfma_f32_16x16x32_bf16 v[24:27], v[188:191], v[220:223], v[24:27]
	v_mfma_f32_16x16x32_bf16 v[16:19], v[196:199], v[220:223], v[16:19]
	v_mfma_f32_16x16x32_bf16 v[8:11], v[188:191], v[228:231], v[8:11]
	v_mfma_f32_16x16x32_bf16 v[0:3], v[196:199], v[228:231], v[0:3]
	s_setprio 0
	s_barrier
	s_add_i32 s36, s36, 2
	s_add_u32 s24, s24, 0x100
	s_addc_u32 s25, s25, 0
	s_add_u32 s19, s19, 0x100
	s_addc_u32 s33, s33, 0
	s_cmp_gt_u32 s36, 29
	s_cbranch_scc0 .LBB0_148
	s_and_b64 vcc, exec, s[14:15]
	s_cbranch_vccz .LBB0_151
	s_barrier

.LBB0_420:
	ds_read_b128 v[146:149], v155
	ds_read_b128 v[158:161], v155 offset:1024
	ds_read_b128 v[162:165], v155 offset:2048
	ds_read_b128 v[166:169], v155 offset:3072
	ds_read_b128 v[170:173], v156
	ds_read_b128 v[174:177], v156 offset:1024
	ds_read_b128 v[178:181], v156 offset:2048
	ds_read_b128 v[182:185], v156 offset:3072
	s_add_u32 s26, s24, 0xfff00080
	s_addc_u32 s27, s25, -1
	s_cmp_eq_u32 s57, 60
	s_cselect_b32 s29, s13, s27
	s_cselect_b32 s28, s19, s26
	s_cselect_b32 s27, s11, s56
	s_cselect_b32 s26, s23, s47
	v_lshl_add_u64 v[150:151], s[24:25], 0, v[138:139]
	s_add_i32 m0, s31, 0xc000
	ds_read_b128 v[186:189], v157
	ds_read_b128 v[190:193], v157 offset:1024
	ds_read_b128 v[194:197], v157 offset:2048
	ds_read_b128 v[198:201], v157 offset:3072
	ds_read_b128 v[202:205], v157 offset:4096
	ds_read_b128 v[206:209], v157 offset:5120
	ds_read_b128 v[210:213], v157 offset:6144
	ds_read_b128 v[214:217], v157 offset:7168
	global_load_lds_dwordx4 v[150:151], off
	v_lshl_add_u64 v[150:151], s[24:25], 0, v[140:141]
	s_add_i32 m0, s31, 0xe000
	s_nop 0
	global_load_lds_dwordx4 v[150:151], off
	s_waitcnt vmcnt(8)
	s_waitcnt lgkmcnt(0)
	s_setprio 1
	s_waitcnt lgkmcnt(0)
	v_mfma_f32_16x16x32_bf16 v[124:127], v[146:149], v[186:189], v[124:127]
	v_mfma_f32_16x16x32_bf16 v[120:123], v[162:165], v[186:189], v[120:123]
	v_mfma_f32_16x16x32_bf16 v[108:111], v[146:149], v[194:197], v[108:111]
	v_mfma_f32_16x16x32_bf16 v[104:107], v[162:165], v[194:197], v[104:107]
	s_barrier
	v_mfma_f32_16x16x32_bf16 v[92:95], v[146:149], v[202:205], v[92:95]
	v_mfma_f32_16x16x32_bf16 v[88:91], v[162:165], v[202:205], v[88:91]
	v_mfma_f32_16x16x32_bf16 v[76:79], v[146:149], v[210:213], v[76:79]
	v_mfma_f32_16x16x32_bf16 v[72:75], v[162:165], v[210:213], v[72:75]
	v_mfma_f32_16x16x32_bf16 v[124:127], v[158:161], v[190:193], v[124:127]
	v_mfma_f32_16x16x32_bf16 v[120:123], v[166:169], v[190:193], v[120:123]
	v_mfma_f32_16x16x32_bf16 v[108:111], v[158:161], v[198:201], v[108:111]
	v_mfma_f32_16x16x32_bf16 v[104:107], v[166:169], v[198:201], v[104:107]
	v_mfma_f32_16x16x32_bf16 v[92:95], v[158:161], v[206:209], v[92:95]
	v_mfma_f32_16x16x32_bf16 v[88:91], v[166:169], v[206:209], v[88:91]
	v_mfma_f32_16x16x32_bf16 v[76:79], v[158:161], v[214:217], v[76:79]
	v_mfma_f32_16x16x32_bf16 v[72:75], v[166:169], v[214:217], v[72:75]
	s_setprio 0
	s_setprio 1
	v_mfma_f32_16x16x32_bf16 v[116:119], v[170:173], v[186:189], v[116:119]
	v_mfma_f32_16x16x32_bf16 v[112:115], v[178:181], v[186:189], v[112:115]
	v_mfma_f32_16x16x32_bf16 v[100:103], v[170:173], v[194:197], v[100:103]
	v_mfma_f32_16x16x32_bf16 v[96:99], v[178:181], v[194:197], v[96:99]
	v_mfma_f32_16x16x32_bf16 v[84:87], v[170:173], v[202:205], v[84:87]
	v_mfma_f32_16x16x32_bf16 v[80:83], v[178:181], v[202:205], v[80:83]
	v_mfma_f32_16x16x32_bf16 v[68:71], v[170:173], v[210:213], v[68:71]
	v_mfma_f32_16x16x32_bf16 v[64:67], v[178:181], v[210:213], v[64:67]
	v_mfma_f32_16x16x32_bf16 v[116:119], v[174:177], v[190:193], v[116:119]
	v_mfma_f32_16x16x32_bf16 v[112:115], v[182:185], v[190:193], v[112:115]
	v_mfma_f32_16x16x32_bf16 v[100:103], v[174:177], v[198:201], v[100:103]
	v_mfma_f32_16x16x32_bf16 v[96:99], v[182:185], v[198:201], v[96:99]
	v_mfma_f32_16x16x32_bf16 v[84:87], v[174:177], v[206:209], v[84:87]
	v_mfma_f32_16x16x32_bf16 v[80:83], v[182:185], v[206:209], v[80:83]
	v_mfma_f32_16x16x32_bf16 v[68:71], v[174:177], v[214:217], v[68:71]
	v_mfma_f32_16x16x32_bf16 v[64:67], v[182:185], v[214:217], v[64:67]
	s_setprio 0
	s_barrier
	s_add_i32 s58, s41, s30
	v_lshl_add_u64 v[150:151], s[26:27], 0, v[130:131]
	s_mov_b32 m0, s58
	ds_read_b128 v[186:189], v157 offset:16384
	ds_read_b128 v[190:193], v157 offset:17408
	ds_read_b128 v[194:197], v157 offset:18432
	ds_read_b128 v[198:201], v157 offset:19456
	ds_read_b128 v[202:205], v157 offset:20480
	ds_read_b128 v[206:209], v157 offset:21504
	ds_read_b128 v[210:213], v157 offset:22528
	ds_read_b128 v[214:217], v157 offset:23552
	global_load_lds_dwordx4 v[150:151], off
	s_add_i32 m0, s58, 0x2000
	s_add_u32 s58, s26, 0x100000
	v_lshl_add_u64 v[218:219], s[26:27], 0, v[134:135]
	s_addc_u32 s59, s27, 0
	s_add_i32 s60, s42, s30
	global_load_lds_dwordx4 v[218:219], off
	v_lshl_add_u64 v[220:221], s[58:59], 0, v[130:131]
	s_mov_b32 m0, s60
	v_lshl_add_u64 v[222:223], s[28:29], 0, v[132:133]
	global_load_lds_dwordx4 v[220:221], off
	v_lshl_add_u64 v[220:221], s[58:59], 0, v[134:135]
	s_add_i32 m0, s60, 0x2000
	s_nop 0
	global_load_lds_dwordx4 v[220:221], off
	v_lshl_add_u64 v[220:221], s[28:29], 0, v[128:129]
	s_mov_b32 m0, s31
	s_nop 0
	global_load_lds_dwordx4 v[220:221], off
	s_mov_b32 m0, s33
	s_nop 0
	global_load_lds_dwordx4 v[222:223], off
	s_waitcnt vmcnt(8)
	s_waitcnt lgkmcnt(0)
	s_setprio 1
	s_waitcnt lgkmcnt(0)
	v_mfma_f32_16x16x32_bf16 v[60:63], v[146:149], v[186:189], v[60:63]
	v_mfma_f32_16x16x32_bf16 v[56:59], v[162:165], v[186:189], v[56:59]
	v_mfma_f32_16x16x32_bf16 v[44:47], v[146:149], v[194:197], v[44:47]
	v_mfma_f32_16x16x32_bf16 v[40:43], v[162:165], v[194:197], v[40:43]
	s_barrier
	v_mfma_f32_16x16x32_bf16 v[28:31], v[146:149], v[202:205], v[28:31]
	v_mfma_f32_16x16x32_bf16 v[24:27], v[162:165], v[202:205], v[24:27]
	v_mfma_f32_16x16x32_bf16 v[12:15], v[146:149], v[210:213], v[12:15]
	v_mfma_f32_16x16x32_bf16 v[8:11], v[162:165], v[210:213], v[8:11]
	v_mfma_f32_16x16x32_bf16 v[60:63], v[158:161], v[190:193], v[60:63]
	v_mfma_f32_16x16x32_bf16 v[56:59], v[166:169], v[190:193], v[56:59]
	v_mfma_f32_16x16x32_bf16 v[44:47], v[158:161], v[198:201], v[44:47]
	v_mfma_f32_16x16x32_bf16 v[40:43], v[166:169], v[198:201], v[40:43]
	v_mfma_f32_16x16x32_bf16 v[28:31], v[158:161], v[206:209], v[28:31]
	v_mfma_f32_16x16x32_bf16 v[24:27], v[166:169], v[206:209], v[24:27]
	v_mfma_f32_16x16x32_bf16 v[12:15], v[158:161], v[214:217], v[12:15]
	v_mfma_f32_16x16x32_bf16 v[8:11], v[166:169], v[214:217], v[8:11]
	s_setprio 0
	s_setprio 1
	v_mfma_f32_16x16x32_bf16 v[52:55], v[170:173], v[186:189], v[52:55]
	v_mfma_f32_16x16x32_bf16 v[48:51], v[178:181], v[186:189], v[48:51]
	v_mfma_f32_16x16x32_bf16 v[36:39], v[170:173], v[194:197], v[36:39]
	v_mfma_f32_16x16x32_bf16 v[32:35], v[178:181], v[194:197], v[32:35]
	v_mfma_f32_16x16x32_bf16 v[20:23], v[170:173], v[202:205], v[20:23]
	v_mfma_f32_16x16x32_bf16 v[16:19], v[178:181], v[202:205], v[16:19]
	v_mfma_f32_16x16x32_bf16 v[4:7], v[170:173], v[210:213], v[4:7]
	v_mfma_f32_16x16x32_bf16 v[0:3], v[178:181], v[210:213], v[0:3]
	v_mfma_f32_16x16x32_bf16 v[52:55], v[174:177], v[190:193], v[52:55]
	v_mfma_f32_16x16x32_bf16 v[48:51], v[182:185], v[190:193], v[48:51]
	v_mfma_f32_16x16x32_bf16 v[36:39], v[174:177], v[198:201], v[36:39]
	v_mfma_f32_16x16x32_bf16 v[32:35], v[182:185], v[198:201], v[32:35]
	v_mfma_f32_16x16x32_bf16 v[20:23], v[174:177], v[206:209], v[20:23]
	v_mfma_f32_16x16x32_bf16 v[16:19], v[182:185], v[206:209], v[16:19]
	v_mfma_f32_16x16x32_bf16 v[4:7], v[174:177], v[214:217], v[4:7]
	v_mfma_f32_16x16x32_bf16 v[0:3], v[182:185], v[214:217], v[0:3]
	s_setprio 0
	s_barrier
	s_add_i32 s58, 0, 0x18000
	v_add_u32_e32 v136, s58, v153
	s_add_i32 s59, 0, 0x1c000
	ds_read_b128 v[146:149], v136
	ds_read_b128 v[158:161], v136 offset:1024
	ds_read_b128 v[162:165], v136 offset:2048
	ds_read_b128 v[166:169], v136 offset:3072
	v_add_u32_e32 v136, s59, v153
	ds_read_b128 v[170:173], v136
	ds_read_b128 v[174:177], v136 offset:1024
	ds_read_b128 v[178:181], v136 offset:2048
	ds_read_b128 v[182:185], v136 offset:3072
	s_add_u32 s28, s28, 0x100000
	s_addc_u32 s29, s29, 0
	s_mov_b32 m0, s34
	v_lshl_add_u64 v[224:225], s[28:29], 0, v[128:129]
	ds_read_b128 v[186:189], v157 offset:32768
	ds_read_b128 v[190:193], v157 offset:33792
	ds_read_b128 v[194:197], v157 offset:34816
	ds_read_b128 v[198:201], v157 offset:35840
	ds_read_b128 v[202:205], v157 offset:36864
	ds_read_b128 v[206:209], v157 offset:37888
	ds_read_b128 v[210:213], v157 offset:38912
	ds_read_b128 v[214:217], v157 offset:39936
	global_load_lds_dwordx4 v[224:225], off
	v_lshl_add_u64 v[224:225], s[28:29], 0, v[132:133]
	s_mov_b32 m0, s35
	s_nop 0
	global_load_lds_dwordx4 v[224:225], off
	s_waitcnt vmcnt(8)
	s_waitcnt lgkmcnt(0)
	s_setprio 1
	s_waitcnt lgkmcnt(0)
	v_mfma_f32_16x16x32_bf16 v[124:127], v[146:149], v[186:189], v[124:127]
	v_mfma_f32_16x16x32_bf16 v[120:123], v[162:165], v[186:189], v[120:123]
	v_mfma_f32_16x16x32_bf16 v[108:111], v[146:149], v[194:197], v[108:111]
	v_mfma_f32_16x16x32_bf16 v[104:107], v[162:165], v[194:197], v[104:107]
	s_barrier
	v_mfma_f32_16x16x32_bf16 v[92:95], v[146:149], v[202:205], v[92:95]
	v_mfma_f32_16x16x32_bf16 v[88:91], v[162:165], v[202:205], v[88:91]
	v_mfma_f32_16x16x32_bf16 v[76:79], v[146:149], v[210:213], v[76:79]
	v_mfma_f32_16x16x32_bf16 v[72:75], v[162:165], v[210:213], v[72:75]
	v_mfma_f32_16x16x32_bf16 v[124:127], v[158:161], v[190:193], v[124:127]
	v_mfma_f32_16x16x32_bf16 v[120:123], v[166:169], v[190:193], v[120:123]
	v_mfma_f32_16x16x32_bf16 v[108:111], v[158:161], v[198:201], v[108:111]
	v_mfma_f32_16x16x32_bf16 v[104:107], v[166:169], v[198:201], v[104:107]
	v_mfma_f32_16x16x32_bf16 v[92:95], v[158:161], v[206:209], v[92:95]
	v_mfma_f32_16x16x32_bf16 v[88:91], v[166:169], v[206:209], v[88:91]
	v_mfma_f32_16x16x32_bf16 v[76:79], v[158:161], v[214:217], v[76:79]
	v_mfma_f32_16x16x32_bf16 v[72:75], v[166:169], v[214:217], v[72:75]
	s_setprio 0
	s_setprio 1
	v_mfma_f32_16x16x32_bf16 v[116:119], v[170:173], v[186:189], v[116:119]
	v_mfma_f32_16x16x32_bf16 v[112:115], v[178:181], v[186:189], v[112:115]
	v_mfma_f32_16x16x32_bf16 v[100:103], v[170:173], v[194:197], v[100:103]
	v_mfma_f32_16x16x32_bf16 v[96:99], v[178:181], v[194:197], v[96:99]
	v_mfma_f32_16x16x32_bf16 v[84:87], v[170:173], v[202:205], v[84:87]
	v_mfma_f32_16x16x32_bf16 v[80:83], v[178:181], v[202:205], v[80:83]
	v_mfma_f32_16x16x32_bf16 v[68:71], v[170:173], v[210:213], v[68:71]
	v_mfma_f32_16x16x32_bf16 v[64:67], v[178:181], v[210:213], v[64:67]
	v_mfma_f32_16x16x32_bf16 v[116:119], v[174:177], v[190:193], v[116:119]
	v_mfma_f32_16x16x32_bf16 v[112:115], v[182:185], v[190:193], v[112:115]
	v_mfma_f32_16x16x32_bf16 v[100:103], v[174:177], v[198:201], v[100:103]
	v_mfma_f32_16x16x32_bf16 v[96:99], v[182:185], v[198:201], v[96:99]
	v_mfma_f32_16x16x32_bf16 v[84:87], v[174:177], v[206:209], v[84:87]
	v_mfma_f32_16x16x32_bf16 v[80:83], v[182:185], v[206:209], v[80:83]
	v_mfma_f32_16x16x32_bf16 v[68:71], v[174:177], v[214:217], v[68:71]
	v_mfma_f32_16x16x32_bf16 v[64:67], v[182:185], v[214:217], v[64:67]
	s_setprio 0
	s_barrier
	s_add_i32 s28, s58, s30
	v_lshl_add_u64 v[150:151], v[150:151], 0, s[6:7]
	s_mov_b32 m0, s28
	ds_read_b128 v[186:189], v157 offset:49152
	ds_read_b128 v[190:193], v157 offset:50176
	ds_read_b128 v[194:197], v157 offset:51200
	ds_read_b128 v[198:201], v157 offset:52224
	ds_read_b128 v[202:205], v157 offset:53248
	ds_read_b128 v[206:209], v157 offset:54272
	ds_read_b128 v[210:213], v157 offset:55296
	ds_read_b128 v[214:217], v157 offset:56320
	global_load_lds_dwordx4 v[150:151], off
	s_add_i32 m0, s28, 0x2000
	s_add_u32 s26, s26, 0x100080
	v_lshl_add_u64 v[150:151], v[218:219], 0, s[6:7]
	s_addc_u32 s27, s27, 0
	s_add_i32 s28, s59, s30
	global_load_lds_dwordx4 v[150:151], off
	v_lshl_add_u64 v[150:151], s[26:27], 0, v[130:131]
	s_mov_b32 m0, s28
	s_nop 0
	global_load_lds_dwordx4 v[150:151], off
	v_lshl_add_u64 v[150:151], s[26:27], 0, v[134:135]
	s_add_i32 m0, s28, 0x2000
	s_nop 0
	global_load_lds_dwordx4 v[150:151], off
	v_lshl_add_u64 v[150:151], v[220:221], 0, s[6:7]
	s_mov_b32 m0, s37
	s_nop 0
	global_load_lds_dwordx4 v[150:151], off
	v_lshl_add_u64 v[150:151], v[222:223], 0, s[6:7]
	s_mov_b32 m0, s38
	s_nop 0
	global_load_lds_dwordx4 v[150:151], off
	s_waitcnt vmcnt(8)
	s_waitcnt lgkmcnt(0)
	s_setprio 1
	s_waitcnt lgkmcnt(0)
	v_mfma_f32_16x16x32_bf16 v[60:63], v[146:149], v[186:189], v[60:63]
	v_mfma_f32_16x16x32_bf16 v[56:59], v[162:165], v[186:189], v[56:59]
	v_mfma_f32_16x16x32_bf16 v[44:47], v[146:149], v[194:197], v[44:47]
	v_mfma_f32_16x16x32_bf16 v[40:43], v[162:165], v[194:197], v[40:43]
	s_barrier
	v_mfma_f32_16x16x32_bf16 v[28:31], v[146:149], v[202:205], v[28:31]
	v_mfma_f32_16x16x32_bf16 v[24:27], v[162:165], v[202:205], v[24:27]
	v_mfma_f32_16x16x32_bf16 v[12:15], v[146:149], v[210:213], v[12:15]
	v_mfma_f32_16x16x32_bf16 v[8:11], v[162:165], v[210:213], v[8:11]
	v_mfma_f32_16x16x32_bf16 v[60:63], v[158:161], v[190:193], v[60:63]
	v_mfma_f32_16x16x32_bf16 v[56:59], v[166:169], v[190:193], v[56:59]
	v_mfma_f32_16x16x32_bf16 v[44:47], v[158:161], v[198:201], v[44:47]
	v_mfma_f32_16x16x32_bf16 v[40:43], v[166:169], v[198:201], v[40:43]
	v_mfma_f32_16x16x32_bf16 v[28:31], v[158:161], v[206:209], v[28:31]
	v_mfma_f32_16x16x32_bf16 v[24:27], v[166:169], v[206:209], v[24:27]
	v_mfma_f32_16x16x32_bf16 v[12:15], v[158:161], v[214:217], v[12:15]
	v_mfma_f32_16x16x32_bf16 v[8:11], v[166:169], v[214:217], v[8:11]
	s_setprio 0
	s_setprio 1
	v_mfma_f32_16x16x32_bf16 v[52:55], v[170:173], v[186:189], v[52:55]
	v_mfma_f32_16x16x32_bf16 v[48:51], v[178:181], v[186:189], v[48:51]
	v_mfma_f32_16x16x32_bf16 v[36:39], v[170:173], v[194:197], v[36:39]
	v_mfma_f32_16x16x32_bf16 v[32:35], v[178:181], v[194:197], v[32:35]
	v_mfma_f32_16x16x32_bf16 v[20:23], v[170:173], v[202:205], v[20:23]
	v_mfma_f32_16x16x32_bf16 v[16:19], v[178:181], v[202:205], v[16:19]
	v_mfma_f32_16x16x32_bf16 v[4:7], v[170:173], v[210:213], v[4:7]
	v_mfma_f32_16x16x32_bf16 v[0:3], v[178:181], v[210:213], v[0:3]
	v_mfma_f32_16x16x32_bf16 v[52:55], v[174:177], v[190:193], v[52:55]
	v_mfma_f32_16x16x32_bf16 v[48:51], v[182:185], v[190:193], v[48:51]
	v_mfma_f32_16x16x32_bf16 v[36:39], v[174:177], v[198:201], v[36:39]
	v_mfma_f32_16x16x32_bf16 v[32:35], v[182:185], v[198:201], v[32:35]
	v_mfma_f32_16x16x32_bf16 v[20:23], v[174:177], v[206:209], v[20:23]
	v_mfma_f32_16x16x32_bf16 v[16:19], v[182:185], v[206:209], v[16:19]
	v_mfma_f32_16x16x32_bf16 v[4:7], v[174:177], v[214:217], v[4:7]
	v_mfma_f32_16x16x32_bf16 v[0:3], v[182:185], v[214:217], v[0:3]
	s_setprio 0
	s_barrier
	s_add_i32 s57, s57, 2
	s_add_u32 s24, s24, 0x100
	s_addc_u32 s25, s25, 0
	s_add_u32 s47, s47, 0x100
	s_addc_u32 s56, s56, 0
	s_cmp_gt_u32 s57, 61
	s_cbranch_scc0 .LBB0_420
	s_and_b64 vcc, exec, s[8:9]
	s_cbranch_vccz .LBB0_423
	s_barrier

.LBB0_700:
	v_add_u32_e32 v130, s81, v161
	ds_read_b128 v[170:173], v130
	ds_read_b128 v[174:177], v130 offset:1024
	ds_read_b128 v[178:181], v130 offset:2048
	ds_read_b128 v[182:185], v130 offset:3072
	v_add_u32_e32 v130, s82, v161
	s_add_u32 s34, s74, s30
	ds_read_b128 v[186:189], v130
	ds_read_b128 v[190:193], v130 offset:1024
	ds_read_b128 v[194:197], v130 offset:2048
	ds_read_b128 v[198:201], v130 offset:3072
	s_addc_u32 s35, s75, s31
	s_add_u32 s40, s34, 0x1b400100
	s_addc_u32 s41, s35, 0
	s_cmpk_eq_i32 s30, 0xf00
	s_cselect_b64 vcc, -1, 0
	v_lshl_add_u64 v[152:153], v[146:147], 0, s[30:31]
	s_and_b64 s[34:35], vcc, exec
	s_cselect_b32 s35, s51, s41
	s_cselect_b32 s34, s50, s40
	v_cndmask_b32_e32 v153, v153, v145, vcc
	v_cndmask_b32_e32 v152, v152, v144, vcc
	v_lshl_add_u64 v[234:235], v[150:151], 0, s[30:31]
	s_add_i32 m0, s38, 0xc000
	ds_read_b128 v[202:205], v162
	ds_read_b128 v[206:209], v162 offset:1024
	ds_read_b128 v[210:213], v162 offset:2048
	ds_read_b128 v[214:217], v162 offset:3072
	ds_read_b128 v[218:221], v162 offset:4096
	ds_read_b128 v[222:225], v162 offset:5120
	ds_read_b128 v[226:229], v162 offset:6144
	ds_read_b128 v[230:233], v162 offset:7168
	global_load_lds_dwordx4 v[234:235], off
	v_lshl_add_u64 v[234:235], v[148:149], 0, s[30:31]
	s_add_i32 m0, s38, 0xe000
	s_nop 0
	global_load_lds_dwordx4 v[234:235], off
	s_waitcnt vmcnt(8)
	s_waitcnt lgkmcnt(0)
	s_setprio 1
	s_waitcnt lgkmcnt(0)
	v_mfma_f32_16x16x32_bf16 v[72:75], v[170:173], v[202:205], v[72:75]
	v_mfma_f32_16x16x32_bf16 v[64:67], v[178:181], v[202:205], v[64:67]
	v_mfma_f32_16x16x32_bf16 v[60:63], v[170:173], v[210:213], v[60:63]
	v_mfma_f32_16x16x32_bf16 v[56:59], v[178:181], v[210:213], v[56:59]
	s_barrier
	v_mfma_f32_16x16x32_bf16 v[52:55], v[170:173], v[218:221], v[52:55]
	v_mfma_f32_16x16x32_bf16 v[48:51], v[178:181], v[218:221], v[48:51]
	v_mfma_f32_16x16x32_bf16 v[44:47], v[170:173], v[226:229], v[44:47]
	v_mfma_f32_16x16x32_bf16 v[40:43], v[178:181], v[226:229], v[40:43]
	v_mfma_f32_16x16x32_bf16 v[72:75], v[174:177], v[206:209], v[72:75]
	v_mfma_f32_16x16x32_bf16 v[64:67], v[182:185], v[206:209], v[64:67]
	v_mfma_f32_16x16x32_bf16 v[60:63], v[174:177], v[214:217], v[60:63]
	v_mfma_f32_16x16x32_bf16 v[56:59], v[182:185], v[214:217], v[56:59]
	v_mfma_f32_16x16x32_bf16 v[52:55], v[174:177], v[222:225], v[52:55]
	v_mfma_f32_16x16x32_bf16 v[48:51], v[182:185], v[222:225], v[48:51]
	v_mfma_f32_16x16x32_bf16 v[44:47], v[174:177], v[230:233], v[44:47]
	v_mfma_f32_16x16x32_bf16 v[40:43], v[182:185], v[230:233], v[40:43]
	s_setprio 0
	s_setprio 1
	v_mfma_f32_16x16x32_bf16 v[36:39], v[186:189], v[202:205], v[36:39]
	v_mfma_f32_16x16x32_bf16 v[32:35], v[194:197], v[202:205], v[32:35]
	v_mfma_f32_16x16x32_bf16 v[28:31], v[186:189], v[210:213], v[28:31]
	v_mfma_f32_16x16x32_bf16 v[24:27], v[194:197], v[210:213], v[24:27]
	v_mfma_f32_16x16x32_bf16 v[20:23], v[186:189], v[218:221], v[20:23]
	v_mfma_f32_16x16x32_bf16 v[16:19], v[194:197], v[218:221], v[16:19]
	v_mfma_f32_16x16x32_bf16 v[12:15], v[186:189], v[226:229], v[12:15]
	v_mfma_f32_16x16x32_bf16 v[8:11], v[194:197], v[226:229], v[8:11]
	v_mfma_f32_16x16x32_bf16 v[36:39], v[190:193], v[206:209], v[36:39]
	v_mfma_f32_16x16x32_bf16 v[32:35], v[198:201], v[206:209], v[32:35]
	v_mfma_f32_16x16x32_bf16 v[28:31], v[190:193], v[214:217], v[28:31]
	v_mfma_f32_16x16x32_bf16 v[24:27], v[198:201], v[214:217], v[24:27]
	v_mfma_f32_16x16x32_bf16 v[20:23], v[190:193], v[222:225], v[20:23]
	v_mfma_f32_16x16x32_bf16 v[16:19], v[198:201], v[222:225], v[16:19]
	v_mfma_f32_16x16x32_bf16 v[12:15], v[190:193], v[230:233], v[12:15]
	v_mfma_f32_16x16x32_bf16 v[8:11], v[198:201], v[230:233], v[8:11]
	s_setprio 0
	s_barrier
	s_add_i32 s40, s81, s37
	v_lshl_add_u64 v[234:235], v[152:153], 0, v[138:139]
	s_mov_b32 m0, s40
	ds_read_b128 v[202:205], v162 offset:16384
	ds_read_b128 v[206:209], v162 offset:17408
	ds_read_b128 v[210:213], v162 offset:18432
	ds_read_b128 v[214:217], v162 offset:19456
	ds_read_b128 v[218:221], v162 offset:20480
	ds_read_b128 v[222:225], v162 offset:21504
	ds_read_b128 v[226:229], v162 offset:22528
	ds_read_b128 v[230:233], v162 offset:23552
	global_load_lds_dwordx4 v[234:235], off
	v_lshl_add_u64 v[236:237], v[152:153], 0, v[140:141]
	s_add_i32 m0, s40, 0x2000
	v_lshl_add_u64 v[238:239], v[152:153], 0, s[10:11]
	s_add_i32 s40, s82, s37
	global_load_lds_dwordx4 v[236:237], off
	v_lshl_add_u64 v[240:241], v[238:239], 0, v[138:139]
	s_mov_b32 m0, s40
	v_lshl_add_u64 v[238:239], v[238:239], 0, v[140:141]
	global_load_lds_dwordx4 v[240:241], off
	s_add_i32 m0, s40, 0x2000
	v_cndmask_b32_e32 v130, v163, v167, vcc
	global_load_lds_dwordx4 v[238:239], off
	s_mov_b32 m0, s38
	v_cndmask_b32_e32 v238, v136, v166, vcc
	global_load_lds_dwordx4 v130, s[34:35]
	s_mov_b32 m0, s39
	v_mov_b32_e32 v239, v131
	global_load_lds_dwordx4 v238, s[34:35]
	s_waitcnt vmcnt(8)
	s_waitcnt lgkmcnt(0)
	v_lshl_add_u64 v[240:241], s[34:35], 0, v[130:131]
	v_lshl_add_u64 v[238:239], s[34:35], 0, v[238:239]
	s_setprio 1
	s_waitcnt lgkmcnt(0)
	v_mfma_f32_16x16x32_bf16 v[4:7], v[170:173], v[202:205], v[4:7]
	v_mfma_f32_16x16x32_bf16 v[0:3], v[178:181], v[202:205], v[0:3]
	v_mfma_f32_16x16x32_bf16 v[68:71], v[170:173], v[210:213], v[68:71]
	v_mfma_f32_16x16x32_bf16 v[76:79], v[178:181], v[210:213], v[76:79]
	s_barrier
	v_mfma_f32_16x16x32_bf16 v[80:83], v[170:173], v[218:221], v[80:83]
	v_mfma_f32_16x16x32_bf16 v[84:87], v[178:181], v[218:221], v[84:87]
	v_mfma_f32_16x16x32_bf16 v[88:91], v[170:173], v[226:229], v[88:91]
	v_mfma_f32_16x16x32_bf16 v[92:95], v[178:181], v[226:229], v[92:95]
	v_mfma_f32_16x16x32_bf16 v[4:7], v[174:177], v[206:209], v[4:7]
	v_mfma_f32_16x16x32_bf16 v[0:3], v[182:185], v[206:209], v[0:3]
	v_mfma_f32_16x16x32_bf16 v[68:71], v[174:177], v[214:217], v[68:71]
	v_mfma_f32_16x16x32_bf16 v[76:79], v[182:185], v[214:217], v[76:79]
	v_mfma_f32_16x16x32_bf16 v[80:83], v[174:177], v[222:225], v[80:83]
	v_mfma_f32_16x16x32_bf16 v[84:87], v[182:185], v[222:225], v[84:87]
	v_mfma_f32_16x16x32_bf16 v[88:91], v[174:177], v[230:233], v[88:91]
	v_mfma_f32_16x16x32_bf16 v[92:95], v[182:185], v[230:233], v[92:95]
	s_setprio 0
	s_setprio 1
	v_mfma_f32_16x16x32_bf16 v[96:99], v[186:189], v[202:205], v[96:99]
	v_mfma_f32_16x16x32_bf16 v[100:103], v[194:197], v[202:205], v[100:103]
	v_mfma_f32_16x16x32_bf16 v[104:107], v[186:189], v[210:213], v[104:107]
	v_mfma_f32_16x16x32_bf16 v[108:111], v[194:197], v[210:213], v[108:111]
	v_mfma_f32_16x16x32_bf16 v[112:115], v[186:189], v[218:221], v[112:115]
	v_mfma_f32_16x16x32_bf16 v[116:119], v[194:197], v[218:221], v[116:119]
	v_mfma_f32_16x16x32_bf16 v[120:123], v[186:189], v[226:229], v[120:123]
	v_mfma_f32_16x16x32_bf16 v[124:127], v[194:197], v[226:229], v[124:127]
	v_mfma_f32_16x16x32_bf16 v[96:99], v[190:193], v[206:209], v[96:99]
	v_mfma_f32_16x16x32_bf16 v[100:103], v[198:201], v[206:209], v[100:103]
	v_mfma_f32_16x16x32_bf16 v[104:107], v[190:193], v[214:217], v[104:107]
	v_mfma_f32_16x16x32_bf16 v[108:111], v[198:201], v[214:217], v[108:111]
	v_mfma_f32_16x16x32_bf16 v[112:115], v[190:193], v[222:225], v[112:115]
	v_mfma_f32_16x16x32_bf16 v[116:119], v[198:201], v[222:225], v[116:119]
	v_mfma_f32_16x16x32_bf16 v[120:123], v[190:193], v[230:233], v[120:123]
	v_mfma_f32_16x16x32_bf16 v[124:127], v[198:201], v[230:233], v[124:127]
	s_setprio 0
	s_barrier
	s_add_i32 s40, 0, 0x18000
	v_add_u32_e32 v130, s40, v161
	s_add_i32 s41, 0, 0x1c000
	ds_read_b128 v[170:173], v130
	ds_read_b128 v[174:177], v130 offset:1024
	ds_read_b128 v[178:181], v130 offset:2048
	ds_read_b128 v[182:185], v130 offset:3072
	v_add_u32_e32 v130, s41, v161
	ds_read_b128 v[186:189], v130
	ds_read_b128 v[190:193], v130 offset:1024
	ds_read_b128 v[194:197], v130 offset:2048
	ds_read_b128 v[198:201], v130 offset:3072
	s_mov_b32 m0, s48
	v_cndmask_b32_e32 v130, v134, v164, vcc
	ds_read_b128 v[202:205], v162 offset:32768
	ds_read_b128 v[206:209], v162 offset:33792
	ds_read_b128 v[210:213], v162 offset:34816
	ds_read_b128 v[214:217], v162 offset:35840
	ds_read_b128 v[218:221], v162 offset:36864
	ds_read_b128 v[222:225], v162 offset:37888
	ds_read_b128 v[226:229], v162 offset:38912
	ds_read_b128 v[230:233], v162 offset:39936
	v_cndmask_b32_e32 v133, v132, v165, vcc
	global_load_lds_dwordx4 v130, s[34:35]
	s_mov_b32 m0, s49
	s_nop 0
	global_load_lds_dwordx4 v133, s[34:35]
	s_waitcnt vmcnt(8)
	s_waitcnt lgkmcnt(0)
	s_setprio 1
	s_waitcnt lgkmcnt(0)
	v_mfma_f32_16x16x32_bf16 v[72:75], v[170:173], v[202:205], v[72:75]
	v_mfma_f32_16x16x32_bf16 v[64:67], v[178:181], v[202:205], v[64:67]
	v_mfma_f32_16x16x32_bf16 v[60:63], v[170:173], v[210:213], v[60:63]
	v_mfma_f32_16x16x32_bf16 v[56:59], v[178:181], v[210:213], v[56:59]
	s_barrier
	v_mfma_f32_16x16x32_bf16 v[52:55], v[170:173], v[218:221], v[52:55]
	v_mfma_f32_16x16x32_bf16 v[48:51], v[178:181], v[218:221], v[48:51]
	v_mfma_f32_16x16x32_bf16 v[44:47], v[170:173], v[226:229], v[44:47]
	v_mfma_f32_16x16x32_bf16 v[40:43], v[178:181], v[226:229], v[40:43]
	v_mfma_f32_16x16x32_bf16 v[72:75], v[174:177], v[206:209], v[72:75]
	v_mfma_f32_16x16x32_bf16 v[64:67], v[182:185], v[206:209], v[64:67]
	v_mfma_f32_16x16x32_bf16 v[60:63], v[174:177], v[214:217], v[60:63]
	v_mfma_f32_16x16x32_bf16 v[56:59], v[182:185], v[214:217], v[56:59]
	v_mfma_f32_16x16x32_bf16 v[52:55], v[174:177], v[222:225], v[52:55]
	v_mfma_f32_16x16x32_bf16 v[48:51], v[182:185], v[222:225], v[48:51]
	v_mfma_f32_16x16x32_bf16 v[44:47], v[174:177], v[230:233], v[44:47]
	v_mfma_f32_16x16x32_bf16 v[40:43], v[182:185], v[230:233], v[40:43]
	s_setprio 0
	s_setprio 1
	v_mfma_f32_16x16x32_bf16 v[36:39], v[186:189], v[202:205], v[36:39]
	v_mfma_f32_16x16x32_bf16 v[32:35], v[194:197], v[202:205], v[32:35]
	v_mfma_f32_16x16x32_bf16 v[28:31], v[186:189], v[210:213], v[28:31]
	v_mfma_f32_16x16x32_bf16 v[24:27], v[194:197], v[210:213], v[24:27]
	v_mfma_f32_16x16x32_bf16 v[20:23], v[186:189], v[218:221], v[20:23]
	v_mfma_f32_16x16x32_bf16 v[16:19], v[194:197], v[218:221], v[16:19]
	v_mfma_f32_16x16x32_bf16 v[12:15], v[186:189], v[226:229], v[12:15]
	v_mfma_f32_16x16x32_bf16 v[8:11], v[194:197], v[226:229], v[8:11]
	v_mfma_f32_16x16x32_bf16 v[36:39], v[190:193], v[206:209], v[36:39]
	v_mfma_f32_16x16x32_bf16 v[32:35], v[198:201], v[206:209], v[32:35]
	v_mfma_f32_16x16x32_bf16 v[28:31], v[190:193], v[214:217], v[28:31]
	v_mfma_f32_16x16x32_bf16 v[24:27], v[198:201], v[214:217], v[24:27]
	v_mfma_f32_16x16x32_bf16 v[20:23], v[190:193], v[222:225], v[20:23]
	v_mfma_f32_16x16x32_bf16 v[16:19], v[198:201], v[222:225], v[16:19]
	v_mfma_f32_16x16x32_bf16 v[12:15], v[190:193], v[230:233], v[12:15]
	v_mfma_f32_16x16x32_bf16 v[8:11], v[198:201], v[230:233], v[8:11]
	s_setprio 0
	s_barrier
	s_add_i32 s34, s40, s37
	v_lshl_add_u64 v[234:235], v[234:235], 0, s[18:19]
	s_mov_b32 m0, s34
	ds_read_b128 v[202:205], v162 offset:49152
	ds_read_b128 v[206:209], v162 offset:50176
	ds_read_b128 v[210:213], v162 offset:51200
	ds_read_b128 v[214:217], v162 offset:52224
	ds_read_b128 v[218:221], v162 offset:53248
	ds_read_b128 v[222:225], v162 offset:54272
	ds_read_b128 v[226:229], v162 offset:55296
	ds_read_b128 v[230:233], v162 offset:56320
	global_load_lds_dwordx4 v[234:235], off
	v_lshl_add_u64 v[234:235], v[236:237], 0, s[18:19]
	s_add_i32 m0, s34, 0x2000
	v_lshl_add_u64 v[152:153], v[152:153], 0, s[24:25]
	s_add_i32 s34, s41, s37
	global_load_lds_dwordx4 v[234:235], off
	v_lshl_add_u64 v[234:235], v[152:153], 0, v[138:139]
	s_mov_b32 m0, s34
	v_lshl_add_u64 v[152:153], v[152:153], 0, v[140:141]
	global_load_lds_dwordx4 v[234:235], off
	s_add_i32 m0, s34, 0x2000
	s_nop 0
	global_load_lds_dwordx4 v[152:153], off
	v_lshl_add_u64 v[152:153], v[240:241], 0, s[18:19]
	s_mov_b32 m0, s54
	s_nop 0
	global_load_lds_dwordx4 v[152:153], off
	v_lshl_add_u64 v[152:153], v[238:239], 0, s[18:19]
	s_mov_b32 m0, s55
	s_nop 0
	global_load_lds_dwordx4 v[152:153], off
	s_waitcnt vmcnt(8)
	s_waitcnt lgkmcnt(0)
	s_setprio 1
	s_waitcnt lgkmcnt(0)
	v_mfma_f32_16x16x32_bf16 v[4:7], v[170:173], v[202:205], v[4:7]
	v_mfma_f32_16x16x32_bf16 v[0:3], v[178:181], v[202:205], v[0:3]
	v_mfma_f32_16x16x32_bf16 v[68:71], v[170:173], v[210:213], v[68:71]
	v_mfma_f32_16x16x32_bf16 v[76:79], v[178:181], v[210:213], v[76:79]
	s_barrier
	v_mfma_f32_16x16x32_bf16 v[80:83], v[170:173], v[218:221], v[80:83]
	v_mfma_f32_16x16x32_bf16 v[84:87], v[178:181], v[218:221], v[84:87]
	v_mfma_f32_16x16x32_bf16 v[88:91], v[170:173], v[226:229], v[88:91]
	v_mfma_f32_16x16x32_bf16 v[92:95], v[178:181], v[226:229], v[92:95]
	v_mfma_f32_16x16x32_bf16 v[4:7], v[174:177], v[206:209], v[4:7]
	v_mfma_f32_16x16x32_bf16 v[0:3], v[182:185], v[206:209], v[0:3]
	v_mfma_f32_16x16x32_bf16 v[68:71], v[174:177], v[214:217], v[68:71]
	v_mfma_f32_16x16x32_bf16 v[76:79], v[182:185], v[214:217], v[76:79]
	v_mfma_f32_16x16x32_bf16 v[80:83], v[174:177], v[222:225], v[80:83]
	v_mfma_f32_16x16x32_bf16 v[84:87], v[182:185], v[222:225], v[84:87]
	v_mfma_f32_16x16x32_bf16 v[88:91], v[174:177], v[230:233], v[88:91]
	v_mfma_f32_16x16x32_bf16 v[92:95], v[182:185], v[230:233], v[92:95]
	s_setprio 0
	s_setprio 1
	v_mfma_f32_16x16x32_bf16 v[96:99], v[186:189], v[202:205], v[96:99]
	v_mfma_f32_16x16x32_bf16 v[100:103], v[194:197], v[202:205], v[100:103]
	v_mfma_f32_16x16x32_bf16 v[104:107], v[186:189], v[210:213], v[104:107]
	v_mfma_f32_16x16x32_bf16 v[108:111], v[194:197], v[210:213], v[108:111]
	v_mfma_f32_16x16x32_bf16 v[112:115], v[186:189], v[218:221], v[112:115]
	v_mfma_f32_16x16x32_bf16 v[116:119], v[194:197], v[218:221], v[116:119]
	v_mfma_f32_16x16x32_bf16 v[120:123], v[186:189], v[226:229], v[120:123]
	v_mfma_f32_16x16x32_bf16 v[124:127], v[194:197], v[226:229], v[124:127]
	v_mfma_f32_16x16x32_bf16 v[96:99], v[190:193], v[206:209], v[96:99]
	v_mfma_f32_16x16x32_bf16 v[100:103], v[198:201], v[206:209], v[100:103]
	v_mfma_f32_16x16x32_bf16 v[104:107], v[190:193], v[214:217], v[104:107]
	v_mfma_f32_16x16x32_bf16 v[108:111], v[198:201], v[214:217], v[108:111]
	v_mfma_f32_16x16x32_bf16 v[112:115], v[190:193], v[222:225], v[112:115]
	v_mfma_f32_16x16x32_bf16 v[116:119], v[198:201], v[222:225], v[116:119]
	v_mfma_f32_16x16x32_bf16 v[120:123], v[190:193], v[230:233], v[120:123]
	v_mfma_f32_16x16x32_bf16 v[124:127], v[198:201], v[230:233], v[124:127]
	s_setprio 0
	s_barrier
	s_add_i32 s33, s33, 2
	s_add_u32 s30, s30, 0x100
	s_addc_u32 s31, s31, 0
	s_cmp_gt_u32 s33, 29
	s_cbranch_scc0 .LBB0_700
	s_and_b64 vcc, exec, s[26:27]
	s_cbranch_vccz .LBB0_703
	s_barrier

.LBB0_840:
	v_add_u32_e32 v161, s54, v157
	ds_read_b128 v[162:165], v161
	ds_read_b128 v[166:169], v161 offset:1024
	ds_read_b128 v[170:173], v161 offset:2048
	ds_read_b128 v[174:177], v161 offset:3072
	v_add_u32_e32 v161, s55, v157
	ds_read_b128 v[178:181], v161
	ds_read_b128 v[182:185], v161 offset:1024
	ds_read_b128 v[186:189], v161 offset:2048
	ds_read_b128 v[190:193], v161 offset:3072
	s_mov_b32 s28, 0xfffe0080
	s_mov_b32 s29, -1
	s_cmp_eq_u32 s58, 4
	v_lshl_add_u64 v[194:195], v[152:153], 0, s[28:29]
	s_cselect_b64 vcc, -1, 0
	v_cndmask_b32_e32 v227, v195, v143, vcc
	v_cndmask_b32_e32 v226, v194, v147, vcc
	v_cndmask_b32_e32 v229, v155, v145, vcc
	v_cndmask_b32_e32 v228, v154, v160, vcc
	v_lshl_add_u64 v[230:231], v[152:153], 0, v[138:139]
	s_add_i32 m0, s33, 0xc000
	ds_read_b128 v[194:197], v159
	ds_read_b128 v[198:201], v159 offset:1024
	ds_read_b128 v[202:205], v159 offset:2048
	ds_read_b128 v[206:209], v159 offset:3072
	ds_read_b128 v[210:213], v159 offset:4096
	ds_read_b128 v[214:217], v159 offset:5120
	ds_read_b128 v[218:221], v159 offset:6144
	ds_read_b128 v[222:225], v159 offset:7168
	global_load_lds_dwordx4 v[230:231], off
	v_lshl_add_u64 v[230:231], v[152:153], 0, v[140:141]
	s_add_i32 m0, s33, 0xe000
	s_nop 0
	global_load_lds_dwordx4 v[230:231], off
	s_waitcnt vmcnt(8)
	s_waitcnt lgkmcnt(0)
	s_setprio 1
	s_waitcnt lgkmcnt(0)
	v_mfma_f32_16x16x32_bf16 v[124:127], v[162:165], v[194:197], v[124:127]
	v_mfma_f32_16x16x32_bf16 v[120:123], v[170:173], v[194:197], v[120:123]
	v_mfma_f32_16x16x32_bf16 v[116:119], v[162:165], v[202:205], v[116:119]
	v_mfma_f32_16x16x32_bf16 v[108:111], v[170:173], v[202:205], v[108:111]
	s_barrier
	v_mfma_f32_16x16x32_bf16 v[100:103], v[162:165], v[210:213], v[100:103]
	v_mfma_f32_16x16x32_bf16 v[92:95], v[170:173], v[210:213], v[92:95]
	v_mfma_f32_16x16x32_bf16 v[80:83], v[162:165], v[218:221], v[80:83]
	v_mfma_f32_16x16x32_bf16 v[72:75], v[170:173], v[218:221], v[72:75]
	v_mfma_f32_16x16x32_bf16 v[124:127], v[166:169], v[198:201], v[124:127]
	v_mfma_f32_16x16x32_bf16 v[120:123], v[174:177], v[198:201], v[120:123]
	v_mfma_f32_16x16x32_bf16 v[116:119], v[166:169], v[206:209], v[116:119]
	v_mfma_f32_16x16x32_bf16 v[108:111], v[174:177], v[206:209], v[108:111]
	v_mfma_f32_16x16x32_bf16 v[100:103], v[166:169], v[214:217], v[100:103]
	v_mfma_f32_16x16x32_bf16 v[92:95], v[174:177], v[214:217], v[92:95]
	v_mfma_f32_16x16x32_bf16 v[80:83], v[166:169], v[222:225], v[80:83]
	v_mfma_f32_16x16x32_bf16 v[72:75], v[174:177], v[222:225], v[72:75]
	s_setprio 0
	s_setprio 1
	v_mfma_f32_16x16x32_bf16 v[112:115], v[178:181], v[194:197], v[112:115]
	v_mfma_f32_16x16x32_bf16 v[104:107], v[186:189], v[194:197], v[104:107]
	v_mfma_f32_16x16x32_bf16 v[96:99], v[178:181], v[202:205], v[96:99]
	v_mfma_f32_16x16x32_bf16 v[88:91], v[186:189], v[202:205], v[88:91]
	v_mfma_f32_16x16x32_bf16 v[84:87], v[178:181], v[210:213], v[84:87]
	v_mfma_f32_16x16x32_bf16 v[76:79], v[186:189], v[210:213], v[76:79]
	v_mfma_f32_16x16x32_bf16 v[68:71], v[178:181], v[218:221], v[68:71]
	v_mfma_f32_16x16x32_bf16 v[64:67], v[186:189], v[218:221], v[64:67]
	v_mfma_f32_16x16x32_bf16 v[112:115], v[182:185], v[198:201], v[112:115]
	v_mfma_f32_16x16x32_bf16 v[104:107], v[190:193], v[198:201], v[104:107]
	v_mfma_f32_16x16x32_bf16 v[96:99], v[182:185], v[206:209], v[96:99]
	v_mfma_f32_16x16x32_bf16 v[88:91], v[190:193], v[206:209], v[88:91]
	v_mfma_f32_16x16x32_bf16 v[84:87], v[182:185], v[214:217], v[84:87]
	v_mfma_f32_16x16x32_bf16 v[76:79], v[190:193], v[214:217], v[76:79]
	v_mfma_f32_16x16x32_bf16 v[68:71], v[182:185], v[222:225], v[68:71]
	v_mfma_f32_16x16x32_bf16 v[64:67], v[190:193], v[222:225], v[64:67]
	s_setprio 0
	s_barrier
	s_add_i32 s28, s54, s31
	v_lshl_add_u64 v[230:231], v[228:229], 0, v[130:131]
	s_mov_b32 m0, s28
	ds_read_b128 v[194:197], v159 offset:16384
	ds_read_b128 v[198:201], v159 offset:17408
	ds_read_b128 v[202:205], v159 offset:18432
	ds_read_b128 v[206:209], v159 offset:19456
	ds_read_b128 v[210:213], v159 offset:20480
	ds_read_b128 v[214:217], v159 offset:21504
	ds_read_b128 v[218:221], v159 offset:22528
	ds_read_b128 v[222:225], v159 offset:23552
	global_load_lds_dwordx4 v[230:231], off
	v_lshl_add_u64 v[232:233], v[228:229], 0, v[134:135]
	s_add_i32 m0, s28, 0x2000
	v_lshl_add_u64 v[234:235], v[228:229], 0, s[10:11]
	s_add_i32 s28, s55, s31
	global_load_lds_dwordx4 v[232:233], off
	v_lshl_add_u64 v[236:237], v[234:235], 0, v[130:131]
	s_mov_b32 m0, s28
	v_lshl_add_u64 v[234:235], v[234:235], 0, v[134:135]
	global_load_lds_dwordx4 v[236:237], off
	s_add_i32 m0, s28, 0x2000
	v_lshl_add_u64 v[236:237], v[226:227], 0, v[132:133]
	global_load_lds_dwordx4 v[234:235], off
	v_lshl_add_u64 v[234:235], v[226:227], 0, v[128:129]
	s_mov_b32 m0, s33
	s_nop 0
	global_load_lds_dwordx4 v[234:235], off
	s_mov_b32 m0, s34
	s_nop 0
	global_load_lds_dwordx4 v[236:237], off
	s_waitcnt vmcnt(8)
	s_waitcnt lgkmcnt(0)
	s_setprio 1
	s_waitcnt lgkmcnt(0)
	v_mfma_f32_16x16x32_bf16 v[60:63], v[162:165], v[194:197], v[60:63]
	v_mfma_f32_16x16x32_bf16 v[56:59], v[170:173], v[194:197], v[56:59]
	v_mfma_f32_16x16x32_bf16 v[52:55], v[162:165], v[202:205], v[52:55]
	v_mfma_f32_16x16x32_bf16 v[44:47], v[170:173], v[202:205], v[44:47]
	s_barrier
	v_mfma_f32_16x16x32_bf16 v[36:39], v[162:165], v[210:213], v[36:39]
	v_mfma_f32_16x16x32_bf16 v[28:31], v[170:173], v[210:213], v[28:31]
	v_mfma_f32_16x16x32_bf16 v[20:23], v[162:165], v[218:221], v[20:23]
	v_mfma_f32_16x16x32_bf16 v[12:15], v[170:173], v[218:221], v[12:15]
	v_mfma_f32_16x16x32_bf16 v[60:63], v[166:169], v[198:201], v[60:63]
	v_mfma_f32_16x16x32_bf16 v[56:59], v[174:177], v[198:201], v[56:59]
	v_mfma_f32_16x16x32_bf16 v[52:55], v[166:169], v[206:209], v[52:55]
	v_mfma_f32_16x16x32_bf16 v[44:47], v[174:177], v[206:209], v[44:47]
	v_mfma_f32_16x16x32_bf16 v[36:39], v[166:169], v[214:217], v[36:39]
	v_mfma_f32_16x16x32_bf16 v[28:31], v[174:177], v[214:217], v[28:31]
	v_mfma_f32_16x16x32_bf16 v[20:23], v[166:169], v[222:225], v[20:23]
	v_mfma_f32_16x16x32_bf16 v[12:15], v[174:177], v[222:225], v[12:15]
	s_setprio 0
	s_setprio 1
	v_mfma_f32_16x16x32_bf16 v[48:51], v[178:181], v[194:197], v[48:51]
	v_mfma_f32_16x16x32_bf16 v[40:43], v[186:189], v[194:197], v[40:43]
	v_mfma_f32_16x16x32_bf16 v[32:35], v[178:181], v[202:205], v[32:35]
	v_mfma_f32_16x16x32_bf16 v[24:27], v[186:189], v[202:205], v[24:27]
	v_mfma_f32_16x16x32_bf16 v[16:19], v[178:181], v[210:213], v[16:19]
	v_mfma_f32_16x16x32_bf16 v[8:11], v[186:189], v[210:213], v[8:11]
	v_mfma_f32_16x16x32_bf16 v[4:7], v[178:181], v[218:221], v[4:7]
	v_mfma_f32_16x16x32_bf16 v[0:3], v[186:189], v[218:221], v[0:3]
	v_mfma_f32_16x16x32_bf16 v[48:51], v[182:185], v[198:201], v[48:51]
	v_mfma_f32_16x16x32_bf16 v[40:43], v[190:193], v[198:201], v[40:43]
	v_mfma_f32_16x16x32_bf16 v[32:35], v[182:185], v[206:209], v[32:35]
	v_mfma_f32_16x16x32_bf16 v[24:27], v[190:193], v[206:209], v[24:27]
	v_mfma_f32_16x16x32_bf16 v[16:19], v[182:185], v[214:217], v[16:19]
	v_mfma_f32_16x16x32_bf16 v[8:11], v[190:193], v[214:217], v[8:11]
	v_mfma_f32_16x16x32_bf16 v[4:7], v[182:185], v[222:225], v[4:7]
	v_mfma_f32_16x16x32_bf16 v[0:3], v[190:193], v[222:225], v[0:3]
	s_setprio 0
	s_barrier
	s_add_i32 s28, 0, 0x18000
	v_add_u32_e32 v161, s28, v157
	s_add_i32 s29, 0, 0x1c000
	ds_read_b128 v[162:165], v161
	ds_read_b128 v[166:169], v161 offset:1024
	ds_read_b128 v[170:173], v161 offset:2048
	ds_read_b128 v[174:177], v161 offset:3072
	v_add_u32_e32 v161, s29, v157
	ds_read_b128 v[178:181], v161
	ds_read_b128 v[182:185], v161 offset:1024
	ds_read_b128 v[186:189], v161 offset:2048
	ds_read_b128 v[190:193], v161 offset:3072
	v_lshl_add_u64 v[226:227], v[226:227], 0, s[10:11]
	s_mov_b32 m0, s35
	v_lshl_add_u64 v[238:239], v[226:227], 0, v[128:129]
	ds_read_b128 v[194:197], v159 offset:32768
	ds_read_b128 v[198:201], v159 offset:33792
	ds_read_b128 v[202:205], v159 offset:34816
	ds_read_b128 v[206:209], v159 offset:35840
	ds_read_b128 v[210:213], v159 offset:36864
	ds_read_b128 v[214:217], v159 offset:37888
	ds_read_b128 v[218:221], v159 offset:38912
	ds_read_b128 v[222:225], v159 offset:39936
	global_load_lds_dwordx4 v[238:239], off
	v_lshl_add_u64 v[226:227], v[226:227], 0, v[132:133]
	s_mov_b32 m0, s36
	s_nop 0
	global_load_lds_dwordx4 v[226:227], off
	s_waitcnt vmcnt(8)
	s_waitcnt lgkmcnt(0)
	s_setprio 1
	s_waitcnt lgkmcnt(0)
	v_mfma_f32_16x16x32_bf16 v[124:127], v[162:165], v[194:197], v[124:127]
	v_mfma_f32_16x16x32_bf16 v[120:123], v[170:173], v[194:197], v[120:123]
	v_mfma_f32_16x16x32_bf16 v[116:119], v[162:165], v[202:205], v[116:119]
	v_mfma_f32_16x16x32_bf16 v[108:111], v[170:173], v[202:205], v[108:111]
	s_barrier
	v_mfma_f32_16x16x32_bf16 v[100:103], v[162:165], v[210:213], v[100:103]
	v_mfma_f32_16x16x32_bf16 v[92:95], v[170:173], v[210:213], v[92:95]
	v_mfma_f32_16x16x32_bf16 v[80:83], v[162:165], v[218:221], v[80:83]
	v_mfma_f32_16x16x32_bf16 v[72:75], v[170:173], v[218:221], v[72:75]
	v_mfma_f32_16x16x32_bf16 v[124:127], v[166:169], v[198:201], v[124:127]
	v_mfma_f32_16x16x32_bf16 v[120:123], v[174:177], v[198:201], v[120:123]
	v_mfma_f32_16x16x32_bf16 v[116:119], v[166:169], v[206:209], v[116:119]
	v_mfma_f32_16x16x32_bf16 v[108:111], v[174:177], v[206:209], v[108:111]
	v_mfma_f32_16x16x32_bf16 v[100:103], v[166:169], v[214:217], v[100:103]
	v_mfma_f32_16x16x32_bf16 v[92:95], v[174:177], v[214:217], v[92:95]
	v_mfma_f32_16x16x32_bf16 v[80:83], v[166:169], v[222:225], v[80:83]
	v_mfma_f32_16x16x32_bf16 v[72:75], v[174:177], v[222:225], v[72:75]
	s_setprio 0
	s_setprio 1
	v_mfma_f32_16x16x32_bf16 v[112:115], v[178:181], v[194:197], v[112:115]
	v_mfma_f32_16x16x32_bf16 v[104:107], v[186:189], v[194:197], v[104:107]
	v_mfma_f32_16x16x32_bf16 v[96:99], v[178:181], v[202:205], v[96:99]
	v_mfma_f32_16x16x32_bf16 v[88:91], v[186:189], v[202:205], v[88:91]
	v_mfma_f32_16x16x32_bf16 v[84:87], v[178:181], v[210:213], v[84:87]
	v_mfma_f32_16x16x32_bf16 v[76:79], v[186:189], v[210:213], v[76:79]
	v_mfma_f32_16x16x32_bf16 v[68:71], v[178:181], v[218:221], v[68:71]
	v_mfma_f32_16x16x32_bf16 v[64:67], v[186:189], v[218:221], v[64:67]
	v_mfma_f32_16x16x32_bf16 v[112:115], v[182:185], v[198:201], v[112:115]
	v_mfma_f32_16x16x32_bf16 v[104:107], v[190:193], v[198:201], v[104:107]
	v_mfma_f32_16x16x32_bf16 v[96:99], v[182:185], v[206:209], v[96:99]
	v_mfma_f32_16x16x32_bf16 v[88:91], v[190:193], v[206:209], v[88:91]
	v_mfma_f32_16x16x32_bf16 v[84:87], v[182:185], v[214:217], v[84:87]
	v_mfma_f32_16x16x32_bf16 v[76:79], v[190:193], v[214:217], v[76:79]
	v_mfma_f32_16x16x32_bf16 v[68:71], v[182:185], v[222:225], v[68:71]
	v_mfma_f32_16x16x32_bf16 v[64:67], v[190:193], v[222:225], v[64:67]
	s_setprio 0
	s_barrier
	s_add_i32 s28, s28, s31
	v_lshl_add_u64 v[226:227], v[230:231], 0, s[14:15]
	s_mov_b32 m0, s28
	ds_read_b128 v[194:197], v159 offset:49152
	ds_read_b128 v[198:201], v159 offset:50176
	ds_read_b128 v[202:205], v159 offset:51200
	ds_read_b128 v[206:209], v159 offset:52224
	ds_read_b128 v[210:213], v159 offset:53248
	ds_read_b128 v[214:217], v159 offset:54272
	ds_read_b128 v[218:221], v159 offset:55296
	ds_read_b128 v[222:225], v159 offset:56320
	global_load_lds_dwordx4 v[226:227], off
	v_lshl_add_u64 v[226:227], v[232:233], 0, s[14:15]
	s_add_i32 m0, s28, 0x2000
	s_add_i32 s28, s29, s31
	global_load_lds_dwordx4 v[226:227], off
	v_lshl_add_u64 v[226:227], v[228:229], 0, s[16:17]
	v_lshl_add_u64 v[228:229], v[226:227], 0, v[130:131]
	s_mov_b32 m0, s28
	v_lshl_add_u64 v[226:227], v[226:227], 0, v[134:135]
	global_load_lds_dwordx4 v[228:229], off
	s_add_i32 m0, s28, 0x2000
	s_nop 0
	global_load_lds_dwordx4 v[226:227], off
	v_lshl_add_u64 v[226:227], v[234:235], 0, s[14:15]
	s_mov_b32 m0, s38
	s_nop 0
	global_load_lds_dwordx4 v[226:227], off
	v_lshl_add_u64 v[226:227], v[236:237], 0, s[14:15]
	s_mov_b32 m0, s39
	s_nop 0
	global_load_lds_dwordx4 v[226:227], off
	s_waitcnt vmcnt(8)
	s_waitcnt lgkmcnt(0)
	s_setprio 1
	s_waitcnt lgkmcnt(0)
	v_mfma_f32_16x16x32_bf16 v[60:63], v[162:165], v[194:197], v[60:63]
	v_mfma_f32_16x16x32_bf16 v[56:59], v[170:173], v[194:197], v[56:59]
	v_mfma_f32_16x16x32_bf16 v[52:55], v[162:165], v[202:205], v[52:55]
	v_mfma_f32_16x16x32_bf16 v[44:47], v[170:173], v[202:205], v[44:47]
	s_barrier
	v_mfma_f32_16x16x32_bf16 v[36:39], v[162:165], v[210:213], v[36:39]
	v_mfma_f32_16x16x32_bf16 v[28:31], v[170:173], v[210:213], v[28:31]
	v_mfma_f32_16x16x32_bf16 v[20:23], v[162:165], v[218:221], v[20:23]
	v_mfma_f32_16x16x32_bf16 v[12:15], v[170:173], v[218:221], v[12:15]
	v_mfma_f32_16x16x32_bf16 v[60:63], v[166:169], v[198:201], v[60:63]
	v_mfma_f32_16x16x32_bf16 v[56:59], v[174:177], v[198:201], v[56:59]
	v_mfma_f32_16x16x32_bf16 v[52:55], v[166:169], v[206:209], v[52:55]
	v_mfma_f32_16x16x32_bf16 v[44:47], v[174:177], v[206:209], v[44:47]
	v_mfma_f32_16x16x32_bf16 v[36:39], v[166:169], v[214:217], v[36:39]
	v_mfma_f32_16x16x32_bf16 v[28:31], v[174:177], v[214:217], v[28:31]
	v_mfma_f32_16x16x32_bf16 v[20:23], v[166:169], v[222:225], v[20:23]
	v_mfma_f32_16x16x32_bf16 v[12:15], v[174:177], v[222:225], v[12:15]
	s_setprio 0
	s_setprio 1
	v_mfma_f32_16x16x32_bf16 v[48:51], v[178:181], v[194:197], v[48:51]
	v_mfma_f32_16x16x32_bf16 v[40:43], v[186:189], v[194:197], v[40:43]
	v_mfma_f32_16x16x32_bf16 v[32:35], v[178:181], v[202:205], v[32:35]
	v_mfma_f32_16x16x32_bf16 v[24:27], v[186:189], v[202:205], v[24:27]
	v_mfma_f32_16x16x32_bf16 v[16:19], v[178:181], v[210:213], v[16:19]
	v_mfma_f32_16x16x32_bf16 v[8:11], v[186:189], v[210:213], v[8:11]
	v_mfma_f32_16x16x32_bf16 v[4:7], v[178:181], v[218:221], v[4:7]
	v_mfma_f32_16x16x32_bf16 v[0:3], v[186:189], v[218:221], v[0:3]
	v_mfma_f32_16x16x32_bf16 v[48:51], v[182:185], v[198:201], v[48:51]
	v_mfma_f32_16x16x32_bf16 v[40:43], v[190:193], v[198:201], v[40:43]
	v_mfma_f32_16x16x32_bf16 v[32:35], v[182:185], v[206:209], v[32:35]
	v_mfma_f32_16x16x32_bf16 v[24:27], v[190:193], v[206:209], v[24:27]
	v_mfma_f32_16x16x32_bf16 v[16:19], v[182:185], v[214:217], v[16:19]
	v_mfma_f32_16x16x32_bf16 v[8:11], v[190:193], v[214:217], v[8:11]
	v_mfma_f32_16x16x32_bf16 v[4:7], v[182:185], v[222:225], v[4:7]
	v_mfma_f32_16x16x32_bf16 v[0:3], v[190:193], v[222:225], v[0:3]
	s_setprio 0
	s_barrier
	s_add_i32 s58, s58, 2
	v_lshl_add_u64 v[152:153], v[152:153], 0, s[22:23]
	s_cmp_gt_u32 s58, 5
	v_lshl_add_u64 v[154:155], v[154:155], 0, s[22:23]
	s_cbranch_scc0 .LBB0_840
	s_and_b64 vcc, exec, s[18:19]
	s_cbranch_vccz .LBB0_843
	s_barrier

.LBB0_1004:
	ds_read_b128 v[152:155], v149
	ds_read_b128 v[156:159], v149 offset:1024
	ds_read_b128 v[160:163], v149 offset:2048
	ds_read_b128 v[164:167], v149 offset:3072
	ds_read_b128 v[168:171], v150
	ds_read_b128 v[172:175], v150 offset:1024
	ds_read_b128 v[176:179], v150 offset:2048
	ds_read_b128 v[180:183], v150 offset:3072
	s_add_u32 s36, s34, 0xfff80080
	s_addc_u32 s37, s35, -1
	s_cmp_eq_u32 s66, 28
	s_cselect_b32 s39, s25, s37
	s_cselect_b32 s38, s62, s36
	s_cselect_b32 s37, s23, s65
	s_cselect_b32 s36, s63, s64
	v_lshl_add_u64 v[144:145], s[34:35], 0, v[136:137]
	s_add_i32 m0, s31, 0xc000
	ds_read_b128 v[184:187], v151
	ds_read_b128 v[188:191], v151 offset:1024
	ds_read_b128 v[192:195], v151 offset:2048
	ds_read_b128 v[196:199], v151 offset:3072
	ds_read_b128 v[200:203], v151 offset:4096
	ds_read_b128 v[204:207], v151 offset:5120
	ds_read_b128 v[208:211], v151 offset:6144
	ds_read_b128 v[212:215], v151 offset:7168
	global_load_lds_dwordx4 v[144:145], off
	v_lshl_add_u64 v[144:145], s[34:35], 0, v[138:139]
	s_add_i32 m0, s31, 0xe000
	s_nop 0
	global_load_lds_dwordx4 v[144:145], off
	s_waitcnt vmcnt(8)
	s_waitcnt lgkmcnt(0)
	s_setprio 1
	s_waitcnt lgkmcnt(0)
	v_mfma_f32_16x16x32_bf16 v[124:127], v[152:155], v[184:187], v[124:127]
	v_mfma_f32_16x16x32_bf16 v[120:123], v[160:163], v[184:187], v[120:123]
	v_mfma_f32_16x16x32_bf16 v[112:115], v[152:155], v[192:195], v[112:115]
	v_mfma_f32_16x16x32_bf16 v[104:107], v[160:163], v[192:195], v[104:107]
	s_barrier
	v_mfma_f32_16x16x32_bf16 v[96:99], v[152:155], v[200:203], v[96:99]
	v_mfma_f32_16x16x32_bf16 v[88:91], v[160:163], v[200:203], v[88:91]
	v_mfma_f32_16x16x32_bf16 v[80:83], v[152:155], v[208:211], v[80:83]
	v_mfma_f32_16x16x32_bf16 v[72:75], v[160:163], v[208:211], v[72:75]
	v_mfma_f32_16x16x32_bf16 v[124:127], v[156:159], v[188:191], v[124:127]
	v_mfma_f32_16x16x32_bf16 v[120:123], v[164:167], v[188:191], v[120:123]
	v_mfma_f32_16x16x32_bf16 v[112:115], v[156:159], v[196:199], v[112:115]
	v_mfma_f32_16x16x32_bf16 v[104:107], v[164:167], v[196:199], v[104:107]
	v_mfma_f32_16x16x32_bf16 v[96:99], v[156:159], v[204:207], v[96:99]
	v_mfma_f32_16x16x32_bf16 v[88:91], v[164:167], v[204:207], v[88:91]
	v_mfma_f32_16x16x32_bf16 v[80:83], v[156:159], v[212:215], v[80:83]
	v_mfma_f32_16x16x32_bf16 v[72:75], v[164:167], v[212:215], v[72:75]
	s_setprio 0
	s_setprio 1
	v_mfma_f32_16x16x32_bf16 v[116:119], v[168:171], v[184:187], v[116:119]
	v_mfma_f32_16x16x32_bf16 v[108:111], v[176:179], v[184:187], v[108:111]
	v_mfma_f32_16x16x32_bf16 v[100:103], v[168:171], v[192:195], v[100:103]
	v_mfma_f32_16x16x32_bf16 v[92:95], v[176:179], v[192:195], v[92:95]
	v_mfma_f32_16x16x32_bf16 v[84:87], v[168:171], v[200:203], v[84:87]
	v_mfma_f32_16x16x32_bf16 v[76:79], v[176:179], v[200:203], v[76:79]
	v_mfma_f32_16x16x32_bf16 v[68:71], v[168:171], v[208:211], v[68:71]
	v_mfma_f32_16x16x32_bf16 v[64:67], v[176:179], v[208:211], v[64:67]
	v_mfma_f32_16x16x32_bf16 v[116:119], v[172:175], v[188:191], v[116:119]
	v_mfma_f32_16x16x32_bf16 v[108:111], v[180:183], v[188:191], v[108:111]
	v_mfma_f32_16x16x32_bf16 v[100:103], v[172:175], v[196:199], v[100:103]
	v_mfma_f32_16x16x32_bf16 v[92:95], v[180:183], v[196:199], v[92:95]
	v_mfma_f32_16x16x32_bf16 v[84:87], v[172:175], v[204:207], v[84:87]
	v_mfma_f32_16x16x32_bf16 v[76:79], v[180:183], v[204:207], v[76:79]
	v_mfma_f32_16x16x32_bf16 v[68:71], v[172:175], v[212:215], v[68:71]
	v_mfma_f32_16x16x32_bf16 v[64:67], v[180:183], v[212:215], v[64:67]
	s_setprio 0
	s_barrier
	s_add_i32 s67, s55, s41
	v_lshl_add_u64 v[144:145], s[36:37], 0, v[132:133]
	s_mov_b32 m0, s67
	ds_read_b128 v[184:187], v151 offset:16384
	ds_read_b128 v[188:191], v151 offset:17408
	ds_read_b128 v[192:195], v151 offset:18432
	ds_read_b128 v[196:199], v151 offset:19456
	ds_read_b128 v[200:203], v151 offset:20480
	ds_read_b128 v[204:207], v151 offset:21504
	ds_read_b128 v[208:211], v151 offset:22528
	ds_read_b128 v[212:215], v151 offset:23552
	global_load_lds_dwordx4 v[144:145], off
	s_add_i32 m0, s67, 0x2000
	s_add_u32 s70, s36, 0x80000
	v_lshl_add_u64 v[216:217], s[36:37], 0, v[128:129]
	s_addc_u32 s71, s37, 0
	s_add_i32 s67, s56, s41
	global_load_lds_dwordx4 v[216:217], off
	v_lshl_add_u64 v[218:219], s[70:71], 0, v[132:133]
	s_mov_b32 m0, s67
	v_lshl_add_u64 v[220:221], s[38:39], 0, v[130:131]
	global_load_lds_dwordx4 v[218:219], off
	v_lshl_add_u64 v[218:219], s[70:71], 0, v[128:129]
	s_add_i32 m0, s67, 0x2000
	s_nop 0
	global_load_lds_dwordx4 v[218:219], off
	v_lshl_add_u64 v[218:219], s[38:39], 0, v[134:135]
	s_mov_b32 m0, s31
	s_nop 0
	global_load_lds_dwordx4 v[218:219], off
	s_mov_b32 m0, s44
	s_nop 0
	global_load_lds_dwordx4 v[220:221], off
	s_waitcnt vmcnt(8)
	s_waitcnt lgkmcnt(0)
	s_setprio 1
	s_waitcnt lgkmcnt(0)
	v_mfma_f32_16x16x32_bf16 v[60:63], v[152:155], v[184:187], v[60:63]
	v_mfma_f32_16x16x32_bf16 v[56:59], v[160:163], v[184:187], v[56:59]
	v_mfma_f32_16x16x32_bf16 v[48:51], v[152:155], v[192:195], v[48:51]
	v_mfma_f32_16x16x32_bf16 v[40:43], v[160:163], v[192:195], v[40:43]
	s_barrier
	v_mfma_f32_16x16x32_bf16 v[32:35], v[152:155], v[200:203], v[32:35]
	v_mfma_f32_16x16x32_bf16 v[24:27], v[160:163], v[200:203], v[24:27]
	v_mfma_f32_16x16x32_bf16 v[16:19], v[152:155], v[208:211], v[16:19]
	v_mfma_f32_16x16x32_bf16 v[8:11], v[160:163], v[208:211], v[8:11]
	v_mfma_f32_16x16x32_bf16 v[60:63], v[156:159], v[188:191], v[60:63]
	v_mfma_f32_16x16x32_bf16 v[56:59], v[164:167], v[188:191], v[56:59]
	v_mfma_f32_16x16x32_bf16 v[48:51], v[156:159], v[196:199], v[48:51]
	v_mfma_f32_16x16x32_bf16 v[40:43], v[164:167], v[196:199], v[40:43]
	v_mfma_f32_16x16x32_bf16 v[32:35], v[156:159], v[204:207], v[32:35]
	v_mfma_f32_16x16x32_bf16 v[24:27], v[164:167], v[204:207], v[24:27]
	v_mfma_f32_16x16x32_bf16 v[16:19], v[156:159], v[212:215], v[16:19]
	v_mfma_f32_16x16x32_bf16 v[8:11], v[164:167], v[212:215], v[8:11]
	s_setprio 0
	s_setprio 1
	v_mfma_f32_16x16x32_bf16 v[52:55], v[168:171], v[184:187], v[52:55]
	v_mfma_f32_16x16x32_bf16 v[44:47], v[176:179], v[184:187], v[44:47]
	v_mfma_f32_16x16x32_bf16 v[36:39], v[168:171], v[192:195], v[36:39]
	v_mfma_f32_16x16x32_bf16 v[28:31], v[176:179], v[192:195], v[28:31]
	v_mfma_f32_16x16x32_bf16 v[20:23], v[168:171], v[200:203], v[20:23]
	v_mfma_f32_16x16x32_bf16 v[12:15], v[176:179], v[200:203], v[12:15]
	v_mfma_f32_16x16x32_bf16 v[4:7], v[168:171], v[208:211], v[4:7]
	v_mfma_f32_16x16x32_bf16 v[0:3], v[176:179], v[208:211], v[0:3]
	v_mfma_f32_16x16x32_bf16 v[52:55], v[172:175], v[188:191], v[52:55]
	v_mfma_f32_16x16x32_bf16 v[44:47], v[180:183], v[188:191], v[44:47]
	v_mfma_f32_16x16x32_bf16 v[36:39], v[172:175], v[196:199], v[36:39]
	v_mfma_f32_16x16x32_bf16 v[28:31], v[180:183], v[196:199], v[28:31]
	v_mfma_f32_16x16x32_bf16 v[20:23], v[172:175], v[204:207], v[20:23]
	v_mfma_f32_16x16x32_bf16 v[12:15], v[180:183], v[204:207], v[12:15]
	v_mfma_f32_16x16x32_bf16 v[4:7], v[172:175], v[212:215], v[4:7]
	v_mfma_f32_16x16x32_bf16 v[0:3], v[180:183], v[212:215], v[0:3]
	s_setprio 0
	s_barrier
	s_add_i32 s67, 0, 0x18000
	s_add_i32 s70, 0, 0x1c000
	v_add_u32_e32 v164, s67, v147
	v_add_u32_e32 v180, s70, v147
	ds_read_b128 v[152:155], v164
	ds_read_b128 v[156:159], v164 offset:1024
	ds_read_b128 v[160:163], v164 offset:2048
	ds_read_b128 v[164:167], v164 offset:3072
	ds_read_b128 v[168:171], v180
	ds_read_b128 v[172:175], v180 offset:1024
	ds_read_b128 v[176:179], v180 offset:2048
	ds_read_b128 v[180:183], v180 offset:3072
	s_add_u32 s38, s38, 0x80000
	s_addc_u32 s39, s39, 0
	s_mov_b32 m0, s45
	v_lshl_add_u64 v[222:223], s[38:39], 0, v[134:135]
	ds_read_b128 v[184:187], v151 offset:32768
	ds_read_b128 v[188:191], v151 offset:33792
	ds_read_b128 v[192:195], v151 offset:34816
	ds_read_b128 v[196:199], v151 offset:35840
	ds_read_b128 v[200:203], v151 offset:36864
	ds_read_b128 v[204:207], v151 offset:37888
	ds_read_b128 v[208:211], v151 offset:38912
	ds_read_b128 v[212:215], v151 offset:39936
	global_load_lds_dwordx4 v[222:223], off
	v_lshl_add_u64 v[222:223], s[38:39], 0, v[130:131]
	s_mov_b32 m0, s46
	s_nop 0
	global_load_lds_dwordx4 v[222:223], off
	s_waitcnt vmcnt(8)
	s_waitcnt lgkmcnt(0)
	s_setprio 1
	s_waitcnt lgkmcnt(0)
	v_mfma_f32_16x16x32_bf16 v[124:127], v[152:155], v[184:187], v[124:127]
	v_mfma_f32_16x16x32_bf16 v[120:123], v[160:163], v[184:187], v[120:123]
	v_mfma_f32_16x16x32_bf16 v[112:115], v[152:155], v[192:195], v[112:115]
	v_mfma_f32_16x16x32_bf16 v[104:107], v[160:163], v[192:195], v[104:107]
	s_barrier
	v_mfma_f32_16x16x32_bf16 v[96:99], v[152:155], v[200:203], v[96:99]
	v_mfma_f32_16x16x32_bf16 v[88:91], v[160:163], v[200:203], v[88:91]
	v_mfma_f32_16x16x32_bf16 v[80:83], v[152:155], v[208:211], v[80:83]
	v_mfma_f32_16x16x32_bf16 v[72:75], v[160:163], v[208:211], v[72:75]
	v_mfma_f32_16x16x32_bf16 v[124:127], v[156:159], v[188:191], v[124:127]
	v_mfma_f32_16x16x32_bf16 v[120:123], v[164:167], v[188:191], v[120:123]
	v_mfma_f32_16x16x32_bf16 v[112:115], v[156:159], v[196:199], v[112:115]
	v_mfma_f32_16x16x32_bf16 v[104:107], v[164:167], v[196:199], v[104:107]
	v_mfma_f32_16x16x32_bf16 v[96:99], v[156:159], v[204:207], v[96:99]
	v_mfma_f32_16x16x32_bf16 v[88:91], v[164:167], v[204:207], v[88:91]
	v_mfma_f32_16x16x32_bf16 v[80:83], v[156:159], v[212:215], v[80:83]
	v_mfma_f32_16x16x32_bf16 v[72:75], v[164:167], v[212:215], v[72:75]
	s_setprio 0
	s_setprio 1
	v_mfma_f32_16x16x32_bf16 v[116:119], v[168:171], v[184:187], v[116:119]
	v_mfma_f32_16x16x32_bf16 v[108:111], v[176:179], v[184:187], v[108:111]
	v_mfma_f32_16x16x32_bf16 v[100:103], v[168:171], v[192:195], v[100:103]
	v_mfma_f32_16x16x32_bf16 v[92:95], v[176:179], v[192:195], v[92:95]
	v_mfma_f32_16x16x32_bf16 v[84:87], v[168:171], v[200:203], v[84:87]
	v_mfma_f32_16x16x32_bf16 v[76:79], v[176:179], v[200:203], v[76:79]
	v_mfma_f32_16x16x32_bf16 v[68:71], v[168:171], v[208:211], v[68:71]
	v_mfma_f32_16x16x32_bf16 v[64:67], v[176:179], v[208:211], v[64:67]
	v_mfma_f32_16x16x32_bf16 v[116:119], v[172:175], v[188:191], v[116:119]
	v_mfma_f32_16x16x32_bf16 v[108:111], v[180:183], v[188:191], v[108:111]
	v_mfma_f32_16x16x32_bf16 v[100:103], v[172:175], v[196:199], v[100:103]
	v_mfma_f32_16x16x32_bf16 v[92:95], v[180:183], v[196:199], v[92:95]
	v_mfma_f32_16x16x32_bf16 v[84:87], v[172:175], v[204:207], v[84:87]
	v_mfma_f32_16x16x32_bf16 v[76:79], v[180:183], v[204:207], v[76:79]
	v_mfma_f32_16x16x32_bf16 v[68:71], v[172:175], v[212:215], v[68:71]
	v_mfma_f32_16x16x32_bf16 v[64:67], v[180:183], v[212:215], v[64:67]
	s_setprio 0
	s_barrier
	s_add_i32 s38, s67, s41
	v_lshl_add_u64 v[144:145], v[144:145], 0, s[8:9]
	s_mov_b32 m0, s38
	ds_read_b128 v[184:187], v151 offset:49152
	ds_read_b128 v[188:191], v151 offset:50176
	ds_read_b128 v[192:195], v151 offset:51200
	ds_read_b128 v[196:199], v151 offset:52224
	ds_read_b128 v[200:203], v151 offset:53248
	ds_read_b128 v[204:207], v151 offset:54272
	ds_read_b128 v[208:211], v151 offset:55296
	ds_read_b128 v[212:215], v151 offset:56320
	global_load_lds_dwordx4 v[144:145], off
	s_add_i32 m0, s38, 0x2000
	s_add_u32 s36, s36, 0x80080
	v_lshl_add_u64 v[144:145], v[216:217], 0, s[8:9]
	s_addc_u32 s37, s37, 0
	s_add_i32 s38, s70, s41
	global_load_lds_dwordx4 v[144:145], off
	v_lshl_add_u64 v[144:145], s[36:37], 0, v[132:133]
	s_mov_b32 m0, s38
	s_nop 0
	global_load_lds_dwordx4 v[144:145], off
	v_lshl_add_u64 v[144:145], s[36:37], 0, v[128:129]
	s_add_i32 m0, s38, 0x2000
	s_nop 0
	global_load_lds_dwordx4 v[144:145], off
	v_lshl_add_u64 v[144:145], v[218:219], 0, s[8:9]
	s_mov_b32 m0, s48
	s_nop 0
	global_load_lds_dwordx4 v[144:145], off
	v_lshl_add_u64 v[144:145], v[220:221], 0, s[8:9]
	s_mov_b32 m0, s49
	s_nop 0
	global_load_lds_dwordx4 v[144:145], off
	s_waitcnt vmcnt(8)
	s_waitcnt lgkmcnt(0)
	s_setprio 1
	s_waitcnt lgkmcnt(0)
	v_mfma_f32_16x16x32_bf16 v[60:63], v[152:155], v[184:187], v[60:63]
	v_mfma_f32_16x16x32_bf16 v[56:59], v[160:163], v[184:187], v[56:59]
	v_mfma_f32_16x16x32_bf16 v[48:51], v[152:155], v[192:195], v[48:51]
	v_mfma_f32_16x16x32_bf16 v[40:43], v[160:163], v[192:195], v[40:43]
	s_barrier
	v_mfma_f32_16x16x32_bf16 v[32:35], v[152:155], v[200:203], v[32:35]
	v_mfma_f32_16x16x32_bf16 v[24:27], v[160:163], v[200:203], v[24:27]
	v_mfma_f32_16x16x32_bf16 v[16:19], v[152:155], v[208:211], v[16:19]
	v_mfma_f32_16x16x32_bf16 v[8:11], v[160:163], v[208:211], v[8:11]
	v_mfma_f32_16x16x32_bf16 v[60:63], v[156:159], v[188:191], v[60:63]
	v_mfma_f32_16x16x32_bf16 v[56:59], v[164:167], v[188:191], v[56:59]
	v_mfma_f32_16x16x32_bf16 v[48:51], v[156:159], v[196:199], v[48:51]
	v_mfma_f32_16x16x32_bf16 v[40:43], v[164:167], v[196:199], v[40:43]
	v_mfma_f32_16x16x32_bf16 v[32:35], v[156:159], v[204:207], v[32:35]
	v_mfma_f32_16x16x32_bf16 v[24:27], v[164:167], v[204:207], v[24:27]
	v_mfma_f32_16x16x32_bf16 v[16:19], v[156:159], v[212:215], v[16:19]
	v_mfma_f32_16x16x32_bf16 v[8:11], v[164:167], v[212:215], v[8:11]
	s_setprio 0
	s_setprio 1
	v_mfma_f32_16x16x32_bf16 v[52:55], v[168:171], v[184:187], v[52:55]
	v_mfma_f32_16x16x32_bf16 v[44:47], v[176:179], v[184:187], v[44:47]
	v_mfma_f32_16x16x32_bf16 v[36:39], v[168:171], v[192:195], v[36:39]
	v_mfma_f32_16x16x32_bf16 v[28:31], v[176:179], v[192:195], v[28:31]
	v_mfma_f32_16x16x32_bf16 v[20:23], v[168:171], v[200:203], v[20:23]
	v_mfma_f32_16x16x32_bf16 v[12:15], v[176:179], v[200:203], v[12:15]
	v_mfma_f32_16x16x32_bf16 v[4:7], v[168:171], v[208:211], v[4:7]
	v_mfma_f32_16x16x32_bf16 v[0:3], v[176:179], v[208:211], v[0:3]
	v_mfma_f32_16x16x32_bf16 v[52:55], v[172:175], v[188:191], v[52:55]
	v_mfma_f32_16x16x32_bf16 v[44:47], v[180:183], v[188:191], v[44:47]
	v_mfma_f32_16x16x32_bf16 v[36:39], v[172:175], v[196:199], v[36:39]
	v_mfma_f32_16x16x32_bf16 v[28:31], v[180:183], v[196:199], v[28:31]
	v_mfma_f32_16x16x32_bf16 v[20:23], v[172:175], v[204:207], v[20:23]
	v_mfma_f32_16x16x32_bf16 v[12:15], v[180:183], v[204:207], v[12:15]
	v_mfma_f32_16x16x32_bf16 v[4:7], v[172:175], v[212:215], v[4:7]
	v_mfma_f32_16x16x32_bf16 v[0:3], v[180:183], v[212:215], v[0:3]
	s_setprio 0
	s_barrier
	s_add_i32 s66, s66, 2
	s_add_u32 s34, s34, 0x100
	s_addc_u32 s35, s35, 0
	s_add_u32 s64, s64, 0x100
	s_addc_u32 s65, s65, 0
	s_cmp_gt_u32 s66, 29
	s_cbranch_scc0 .LBB0_1004
	s_and_b64 vcc, exec, s[10:11]
	s_cbranch_vccz .LBB0_1007
	s_barrier

.LBB0_1329:
	ds_read_b128 v[144:147], v151
	ds_read_b128 v[154:157], v151 offset:1024
	ds_read_b128 v[158:161], v151 offset:2048
	ds_read_b128 v[162:165], v151 offset:3072
	ds_read_b128 v[166:169], v152
	ds_read_b128 v[170:173], v152 offset:1024
	ds_read_b128 v[174:177], v152 offset:2048
	ds_read_b128 v[178:181], v152 offset:3072
	s_add_u32 s36, s34, 0xfff80080
	s_addc_u32 s37, s35, -1
	s_cmp_eq_u32 s63, 28
	s_cselect_b32 s39, s25, s37
	s_cselect_b32 s38, s59, s36
	s_cselect_b32 s37, s23, s62
	s_cselect_b32 s36, s60, s61
	v_lshl_add_u64 v[214:215], s[34:35], 0, v[136:137]
	s_add_i32 m0, s31, 0xc000
	ds_read_b128 v[182:185], v153
	ds_read_b128 v[186:189], v153 offset:1024
	ds_read_b128 v[190:193], v153 offset:2048
	ds_read_b128 v[194:197], v153 offset:3072
	ds_read_b128 v[198:201], v153 offset:4096
	ds_read_b128 v[202:205], v153 offset:5120
	ds_read_b128 v[206:209], v153 offset:6144
	ds_read_b128 v[210:213], v153 offset:7168
	global_load_lds_dwordx4 v[214:215], off
	v_lshl_add_u64 v[214:215], s[34:35], 0, v[138:139]
	s_add_i32 m0, s31, 0xe000
	s_nop 0
	global_load_lds_dwordx4 v[214:215], off
	s_waitcnt vmcnt(8)
	s_waitcnt lgkmcnt(0)
	s_setprio 1
	s_waitcnt lgkmcnt(0)
	v_mfma_f32_16x16x32_bf16 v[124:127], v[144:147], v[182:185], v[124:127]
	v_mfma_f32_16x16x32_bf16 v[120:123], v[158:161], v[182:185], v[120:123]
	v_mfma_f32_16x16x32_bf16 v[112:115], v[144:147], v[190:193], v[112:115]
	v_mfma_f32_16x16x32_bf16 v[104:107], v[158:161], v[190:193], v[104:107]
	s_barrier
	v_mfma_f32_16x16x32_bf16 v[96:99], v[144:147], v[198:201], v[96:99]
	v_mfma_f32_16x16x32_bf16 v[88:91], v[158:161], v[198:201], v[88:91]
	v_mfma_f32_16x16x32_bf16 v[80:83], v[144:147], v[206:209], v[80:83]
	v_mfma_f32_16x16x32_bf16 v[72:75], v[158:161], v[206:209], v[72:75]
	v_mfma_f32_16x16x32_bf16 v[124:127], v[154:157], v[186:189], v[124:127]
	v_mfma_f32_16x16x32_bf16 v[120:123], v[162:165], v[186:189], v[120:123]
	v_mfma_f32_16x16x32_bf16 v[112:115], v[154:157], v[194:197], v[112:115]
	v_mfma_f32_16x16x32_bf16 v[104:107], v[162:165], v[194:197], v[104:107]
	v_mfma_f32_16x16x32_bf16 v[96:99], v[154:157], v[202:205], v[96:99]
	v_mfma_f32_16x16x32_bf16 v[88:91], v[162:165], v[202:205], v[88:91]
	v_mfma_f32_16x16x32_bf16 v[80:83], v[154:157], v[210:213], v[80:83]
	v_mfma_f32_16x16x32_bf16 v[72:75], v[162:165], v[210:213], v[72:75]
	s_setprio 0
	s_setprio 1
	v_mfma_f32_16x16x32_bf16 v[116:119], v[166:169], v[182:185], v[116:119]
	v_mfma_f32_16x16x32_bf16 v[108:111], v[174:177], v[182:185], v[108:111]
	v_mfma_f32_16x16x32_bf16 v[100:103], v[166:169], v[190:193], v[100:103]
	v_mfma_f32_16x16x32_bf16 v[92:95], v[174:177], v[190:193], v[92:95]
	v_mfma_f32_16x16x32_bf16 v[84:87], v[166:169], v[198:201], v[84:87]
	v_mfma_f32_16x16x32_bf16 v[76:79], v[174:177], v[198:201], v[76:79]
	v_mfma_f32_16x16x32_bf16 v[68:71], v[166:169], v[206:209], v[68:71]
	v_mfma_f32_16x16x32_bf16 v[64:67], v[174:177], v[206:209], v[64:67]
	v_mfma_f32_16x16x32_bf16 v[116:119], v[170:173], v[186:189], v[116:119]
	v_mfma_f32_16x16x32_bf16 v[108:111], v[178:181], v[186:189], v[108:111]
	v_mfma_f32_16x16x32_bf16 v[100:103], v[170:173], v[194:197], v[100:103]
	v_mfma_f32_16x16x32_bf16 v[92:95], v[178:181], v[194:197], v[92:95]
	v_mfma_f32_16x16x32_bf16 v[84:87], v[170:173], v[202:205], v[84:87]
	v_mfma_f32_16x16x32_bf16 v[76:79], v[178:181], v[202:205], v[76:79]
	v_mfma_f32_16x16x32_bf16 v[68:71], v[170:173], v[210:213], v[68:71]
	v_mfma_f32_16x16x32_bf16 v[64:67], v[178:181], v[210:213], v[64:67]
	s_setprio 0
	s_barrier
	s_add_i32 s64, s48, s40
	v_lshl_add_u64 v[214:215], s[36:37], 0, v[130:131]
	s_mov_b32 m0, s64
	ds_read_b128 v[182:185], v153 offset:16384
	ds_read_b128 v[186:189], v153 offset:17408
	ds_read_b128 v[190:193], v153 offset:18432
	ds_read_b128 v[194:197], v153 offset:19456
	ds_read_b128 v[198:201], v153 offset:20480
	ds_read_b128 v[202:205], v153 offset:21504
	ds_read_b128 v[206:209], v153 offset:22528
	ds_read_b128 v[210:213], v153 offset:23552
	global_load_lds_dwordx4 v[214:215], off
	s_add_i32 m0, s64, 0x2000
	s_add_u32 s64, s36, 0x80000
	v_lshl_add_u64 v[216:217], s[36:37], 0, v[134:135]
	s_addc_u32 s65, s37, 0
	s_add_i32 s66, s49, s40
	global_load_lds_dwordx4 v[216:217], off
	v_lshl_add_u64 v[218:219], s[64:65], 0, v[130:131]
	s_mov_b32 m0, s66
	v_lshl_add_u64 v[220:221], s[38:39], 0, v[132:133]
	global_load_lds_dwordx4 v[218:219], off
	v_lshl_add_u64 v[218:219], s[64:65], 0, v[134:135]
	s_add_i32 m0, s66, 0x2000
	s_nop 0
	global_load_lds_dwordx4 v[218:219], off
	v_lshl_add_u64 v[218:219], s[38:39], 0, v[128:129]
	s_mov_b32 m0, s31
	s_nop 0
	global_load_lds_dwordx4 v[218:219], off
	s_mov_b32 m0, s41
	s_nop 0
	global_load_lds_dwordx4 v[220:221], off
	s_waitcnt vmcnt(8)
	s_waitcnt lgkmcnt(0)
	s_setprio 1
	s_waitcnt lgkmcnt(0)
	v_mfma_f32_16x16x32_bf16 v[60:63], v[144:147], v[182:185], v[60:63]
	v_mfma_f32_16x16x32_bf16 v[56:59], v[158:161], v[182:185], v[56:59]
	v_mfma_f32_16x16x32_bf16 v[44:47], v[144:147], v[190:193], v[44:47]
	v_mfma_f32_16x16x32_bf16 v[40:43], v[158:161], v[190:193], v[40:43]
	s_barrier
	v_mfma_f32_16x16x32_bf16 v[28:31], v[144:147], v[198:201], v[28:31]
	v_mfma_f32_16x16x32_bf16 v[24:27], v[158:161], v[198:201], v[24:27]
	v_mfma_f32_16x16x32_bf16 v[12:15], v[144:147], v[206:209], v[12:15]
	v_mfma_f32_16x16x32_bf16 v[8:11], v[158:161], v[206:209], v[8:11]
	v_mfma_f32_16x16x32_bf16 v[60:63], v[154:157], v[186:189], v[60:63]
	v_mfma_f32_16x16x32_bf16 v[56:59], v[162:165], v[186:189], v[56:59]
	v_mfma_f32_16x16x32_bf16 v[44:47], v[154:157], v[194:197], v[44:47]
	v_mfma_f32_16x16x32_bf16 v[40:43], v[162:165], v[194:197], v[40:43]
	v_mfma_f32_16x16x32_bf16 v[28:31], v[154:157], v[202:205], v[28:31]
	v_mfma_f32_16x16x32_bf16 v[24:27], v[162:165], v[202:205], v[24:27]
	v_mfma_f32_16x16x32_bf16 v[12:15], v[154:157], v[210:213], v[12:15]
	v_mfma_f32_16x16x32_bf16 v[8:11], v[162:165], v[210:213], v[8:11]
	s_setprio 0
	s_setprio 1
	v_mfma_f32_16x16x32_bf16 v[52:55], v[166:169], v[182:185], v[52:55]
	v_mfma_f32_16x16x32_bf16 v[48:51], v[174:177], v[182:185], v[48:51]
	v_mfma_f32_16x16x32_bf16 v[36:39], v[166:169], v[190:193], v[36:39]
	v_mfma_f32_16x16x32_bf16 v[32:35], v[174:177], v[190:193], v[32:35]
	v_mfma_f32_16x16x32_bf16 v[20:23], v[166:169], v[198:201], v[20:23]
	v_mfma_f32_16x16x32_bf16 v[16:19], v[174:177], v[198:201], v[16:19]
	v_mfma_f32_16x16x32_bf16 v[4:7], v[166:169], v[206:209], v[4:7]
	v_mfma_f32_16x16x32_bf16 v[0:3], v[174:177], v[206:209], v[0:3]
	v_mfma_f32_16x16x32_bf16 v[52:55], v[170:173], v[186:189], v[52:55]
	v_mfma_f32_16x16x32_bf16 v[48:51], v[178:181], v[186:189], v[48:51]
	v_mfma_f32_16x16x32_bf16 v[36:39], v[170:173], v[194:197], v[36:39]
	v_mfma_f32_16x16x32_bf16 v[32:35], v[178:181], v[194:197], v[32:35]
	v_mfma_f32_16x16x32_bf16 v[20:23], v[170:173], v[202:205], v[20:23]
	v_mfma_f32_16x16x32_bf16 v[16:19], v[178:181], v[202:205], v[16:19]
	v_mfma_f32_16x16x32_bf16 v[4:7], v[170:173], v[210:213], v[4:7]
	v_mfma_f32_16x16x32_bf16 v[0:3], v[178:181], v[210:213], v[0:3]
	s_setprio 0
	s_barrier
	s_add_i32 s64, 0, 0x18000
	s_add_i32 s65, 0, 0x1c000
	v_add_u32_e32 v162, s64, v149
	v_add_u32_e32 v178, s65, v149
	ds_read_b128 v[144:147], v162
	ds_read_b128 v[154:157], v162 offset:1024
	ds_read_b128 v[158:161], v162 offset:2048
	ds_read_b128 v[162:165], v162 offset:3072
	ds_read_b128 v[166:169], v178
	ds_read_b128 v[170:173], v178 offset:1024
	ds_read_b128 v[174:177], v178 offset:2048
	ds_read_b128 v[178:181], v178 offset:3072
	s_add_u32 s38, s38, 0x80000
	s_addc_u32 s39, s39, 0
	s_mov_b32 m0, s42
	v_lshl_add_u64 v[222:223], s[38:39], 0, v[128:129]
	ds_read_b128 v[182:185], v153 offset:32768
	ds_read_b128 v[186:189], v153 offset:33792
	ds_read_b128 v[190:193], v153 offset:34816
	ds_read_b128 v[194:197], v153 offset:35840
	ds_read_b128 v[198:201], v153 offset:36864
	ds_read_b128 v[202:205], v153 offset:37888
	ds_read_b128 v[206:209], v153 offset:38912
	ds_read_b128 v[210:213], v153 offset:39936
	global_load_lds_dwordx4 v[222:223], off
	v_lshl_add_u64 v[222:223], s[38:39], 0, v[132:133]
	s_mov_b32 m0, s43
	s_nop 0
	global_load_lds_dwordx4 v[222:223], off
	s_waitcnt vmcnt(8)
	s_waitcnt lgkmcnt(0)
	s_setprio 1
	s_waitcnt lgkmcnt(0)
	v_mfma_f32_16x16x32_bf16 v[124:127], v[144:147], v[182:185], v[124:127]
	v_mfma_f32_16x16x32_bf16 v[120:123], v[158:161], v[182:185], v[120:123]
	v_mfma_f32_16x16x32_bf16 v[112:115], v[144:147], v[190:193], v[112:115]
	v_mfma_f32_16x16x32_bf16 v[104:107], v[158:161], v[190:193], v[104:107]
	s_barrier
	v_mfma_f32_16x16x32_bf16 v[96:99], v[144:147], v[198:201], v[96:99]
	v_mfma_f32_16x16x32_bf16 v[88:91], v[158:161], v[198:201], v[88:91]
	v_mfma_f32_16x16x32_bf16 v[80:83], v[144:147], v[206:209], v[80:83]
	v_mfma_f32_16x16x32_bf16 v[72:75], v[158:161], v[206:209], v[72:75]
	v_mfma_f32_16x16x32_bf16 v[124:127], v[154:157], v[186:189], v[124:127]
	v_mfma_f32_16x16x32_bf16 v[120:123], v[162:165], v[186:189], v[120:123]
	v_mfma_f32_16x16x32_bf16 v[112:115], v[154:157], v[194:197], v[112:115]
	v_mfma_f32_16x16x32_bf16 v[104:107], v[162:165], v[194:197], v[104:107]
	v_mfma_f32_16x16x32_bf16 v[96:99], v[154:157], v[202:205], v[96:99]
	v_mfma_f32_16x16x32_bf16 v[88:91], v[162:165], v[202:205], v[88:91]
	v_mfma_f32_16x16x32_bf16 v[80:83], v[154:157], v[210:213], v[80:83]
	v_mfma_f32_16x16x32_bf16 v[72:75], v[162:165], v[210:213], v[72:75]
	s_setprio 0
	s_setprio 1
	v_mfma_f32_16x16x32_bf16 v[116:119], v[166:169], v[182:185], v[116:119]
	v_mfma_f32_16x16x32_bf16 v[108:111], v[174:177], v[182:185], v[108:111]
	v_mfma_f32_16x16x32_bf16 v[100:103], v[166:169], v[190:193], v[100:103]
	v_mfma_f32_16x16x32_bf16 v[92:95], v[174:177], v[190:193], v[92:95]
	v_mfma_f32_16x16x32_bf16 v[84:87], v[166:169], v[198:201], v[84:87]
	v_mfma_f32_16x16x32_bf16 v[76:79], v[174:177], v[198:201], v[76:79]
	v_mfma_f32_16x16x32_bf16 v[68:71], v[166:169], v[206:209], v[68:71]
	v_mfma_f32_16x16x32_bf16 v[64:67], v[174:177], v[206:209], v[64:67]
	v_mfma_f32_16x16x32_bf16 v[116:119], v[170:173], v[186:189], v[116:119]
	v_mfma_f32_16x16x32_bf16 v[108:111], v[178:181], v[186:189], v[108:111]
	v_mfma_f32_16x16x32_bf16 v[100:103], v[170:173], v[194:197], v[100:103]
	v_mfma_f32_16x16x32_bf16 v[92:95], v[178:181], v[194:197], v[92:95]
	v_mfma_f32_16x16x32_bf16 v[84:87], v[170:173], v[202:205], v[84:87]
	v_mfma_f32_16x16x32_bf16 v[76:79], v[178:181], v[202:205], v[76:79]
	v_mfma_f32_16x16x32_bf16 v[68:71], v[170:173], v[210:213], v[68:71]
	v_mfma_f32_16x16x32_bf16 v[64:67], v[178:181], v[210:213], v[64:67]
	s_setprio 0
	s_barrier
	s_add_i32 s38, s64, s40
	v_lshl_add_u64 v[214:215], v[214:215], 0, s[10:11]
	s_mov_b32 m0, s38
	ds_read_b128 v[182:185], v153 offset:49152
	ds_read_b128 v[186:189], v153 offset:50176
	ds_read_b128 v[190:193], v153 offset:51200
	ds_read_b128 v[194:197], v153 offset:52224
	ds_read_b128 v[198:201], v153 offset:53248
	ds_read_b128 v[202:205], v153 offset:54272
	ds_read_b128 v[206:209], v153 offset:55296
	ds_read_b128 v[210:213], v153 offset:56320
	global_load_lds_dwordx4 v[214:215], off
	s_add_i32 m0, s38, 0x2000
	s_add_u32 s36, s36, 0x80080
	v_lshl_add_u64 v[214:215], v[216:217], 0, s[10:11]
	s_addc_u32 s37, s37, 0
	s_add_i32 s38, s65, s40
	global_load_lds_dwordx4 v[214:215], off
	v_lshl_add_u64 v[214:215], s[36:37], 0, v[130:131]
	s_mov_b32 m0, s38
	s_nop 0
	global_load_lds_dwordx4 v[214:215], off
	v_lshl_add_u64 v[214:215], s[36:37], 0, v[134:135]
	s_add_i32 m0, s38, 0x2000
	s_nop 0
	global_load_lds_dwordx4 v[214:215], off
	v_lshl_add_u64 v[214:215], v[218:219], 0, s[10:11]
	s_mov_b32 m0, s45
	s_nop 0
	global_load_lds_dwordx4 v[214:215], off
	v_lshl_add_u64 v[214:215], v[220:221], 0, s[10:11]
	s_mov_b32 m0, s46
	s_nop 0
	global_load_lds_dwordx4 v[214:215], off
	s_waitcnt vmcnt(8)
	s_waitcnt lgkmcnt(0)
	s_setprio 1
	s_waitcnt lgkmcnt(0)
	v_mfma_f32_16x16x32_bf16 v[60:63], v[144:147], v[182:185], v[60:63]
	v_mfma_f32_16x16x32_bf16 v[56:59], v[158:161], v[182:185], v[56:59]
	v_mfma_f32_16x16x32_bf16 v[44:47], v[144:147], v[190:193], v[44:47]
	v_mfma_f32_16x16x32_bf16 v[40:43], v[158:161], v[190:193], v[40:43]
	s_barrier
	v_mfma_f32_16x16x32_bf16 v[28:31], v[144:147], v[198:201], v[28:31]
	v_mfma_f32_16x16x32_bf16 v[24:27], v[158:161], v[198:201], v[24:27]
	v_mfma_f32_16x16x32_bf16 v[12:15], v[144:147], v[206:209], v[12:15]
	v_mfma_f32_16x16x32_bf16 v[8:11], v[158:161], v[206:209], v[8:11]
	v_mfma_f32_16x16x32_bf16 v[60:63], v[154:157], v[186:189], v[60:63]
	v_mfma_f32_16x16x32_bf16 v[56:59], v[162:165], v[186:189], v[56:59]
	v_mfma_f32_16x16x32_bf16 v[44:47], v[154:157], v[194:197], v[44:47]
	v_mfma_f32_16x16x32_bf16 v[40:43], v[162:165], v[194:197], v[40:43]
	v_mfma_f32_16x16x32_bf16 v[28:31], v[154:157], v[202:205], v[28:31]
	v_mfma_f32_16x16x32_bf16 v[24:27], v[162:165], v[202:205], v[24:27]
	v_mfma_f32_16x16x32_bf16 v[12:15], v[154:157], v[210:213], v[12:15]
	v_mfma_f32_16x16x32_bf16 v[8:11], v[162:165], v[210:213], v[8:11]
	s_setprio 0
	s_setprio 1
	v_mfma_f32_16x16x32_bf16 v[52:55], v[166:169], v[182:185], v[52:55]
	v_mfma_f32_16x16x32_bf16 v[48:51], v[174:177], v[182:185], v[48:51]
	v_mfma_f32_16x16x32_bf16 v[36:39], v[166:169], v[190:193], v[36:39]
	v_mfma_f32_16x16x32_bf16 v[32:35], v[174:177], v[190:193], v[32:35]
	v_mfma_f32_16x16x32_bf16 v[20:23], v[166:169], v[198:201], v[20:23]
	v_mfma_f32_16x16x32_bf16 v[16:19], v[174:177], v[198:201], v[16:19]
	v_mfma_f32_16x16x32_bf16 v[4:7], v[166:169], v[206:209], v[4:7]
	v_mfma_f32_16x16x32_bf16 v[0:3], v[174:177], v[206:209], v[0:3]
	v_mfma_f32_16x16x32_bf16 v[52:55], v[170:173], v[186:189], v[52:55]
	v_mfma_f32_16x16x32_bf16 v[48:51], v[178:181], v[186:189], v[48:51]
	v_mfma_f32_16x16x32_bf16 v[36:39], v[170:173], v[194:197], v[36:39]
	v_mfma_f32_16x16x32_bf16 v[32:35], v[178:181], v[194:197], v[32:35]
	v_mfma_f32_16x16x32_bf16 v[20:23], v[170:173], v[202:205], v[20:23]
	v_mfma_f32_16x16x32_bf16 v[16:19], v[178:181], v[202:205], v[16:19]
	v_mfma_f32_16x16x32_bf16 v[4:7], v[170:173], v[210:213], v[4:7]
	v_mfma_f32_16x16x32_bf16 v[0:3], v[178:181], v[210:213], v[0:3]
	s_setprio 0
	s_barrier
	s_add_i32 s63, s63, 2
	s_add_u32 s34, s34, 0x100
	s_addc_u32 s35, s35, 0
	s_add_u32 s61, s61, 0x100
	s_addc_u32 s62, s62, 0
	s_cmp_gt_u32 s63, 29
	s_cbranch_scc0 .LBB0_1329
	s_and_b64 vcc, exec, s[12:13]
	s_mov_b32 s60, s78
	s_cbranch_vccz .LBB0_1332
	s_barrier

.LBB0_1576:
	v_add_u32_e32 v130, s67, v159
	ds_read_b128 v[168:171], v130
	ds_read_b128 v[172:175], v130 offset:1024
	ds_read_b128 v[176:179], v130 offset:2048
	ds_read_b128 v[180:183], v130 offset:3072
	v_add_u32_e32 v130, s68, v159
	s_add_u32 s38, s74, s36
	ds_read_b128 v[184:187], v130
	ds_read_b128 v[188:191], v130 offset:1024
	ds_read_b128 v[192:195], v130 offset:2048
	ds_read_b128 v[196:199], v130 offset:3072
	s_addc_u32 s39, s75, s37
	s_add_u32 s45, s38, 0x1b400100
	s_addc_u32 s46, s39, 0
	s_cmpk_eq_i32 s36, 0xf00
	s_cselect_b64 vcc, -1, 0
	v_lshl_add_u64 v[200:201], v[146:147], 0, s[36:37]
	s_and_b64 s[38:39], vcc, exec
	v_cndmask_b32_e32 v233, v201, v145, vcc
	s_cselect_b32 s39, s51, s46
	s_cselect_b32 s38, s50, s45
	v_cndmask_b32_e32 v232, v200, v144, vcc
	v_lshl_add_u64 v[234:235], v[150:151], 0, s[36:37]
	s_add_i32 m0, s42, 0xc000
	ds_read_b128 v[200:203], v160
	ds_read_b128 v[204:207], v160 offset:1024
	ds_read_b128 v[208:211], v160 offset:2048
	ds_read_b128 v[212:215], v160 offset:3072
	ds_read_b128 v[216:219], v160 offset:4096
	ds_read_b128 v[220:223], v160 offset:5120
	ds_read_b128 v[224:227], v160 offset:6144
	ds_read_b128 v[228:231], v160 offset:7168
	global_load_lds_dwordx4 v[234:235], off
	v_lshl_add_u64 v[234:235], v[148:149], 0, s[36:37]
	s_add_i32 m0, s42, 0xe000
	s_nop 0
	global_load_lds_dwordx4 v[234:235], off
	s_waitcnt vmcnt(8)
	s_waitcnt lgkmcnt(0)
	s_setprio 1
	s_waitcnt lgkmcnt(0)
	v_mfma_f32_16x16x32_bf16 v[72:75], v[168:171], v[200:203], v[72:75]
	v_mfma_f32_16x16x32_bf16 v[64:67], v[176:179], v[200:203], v[64:67]
	v_mfma_f32_16x16x32_bf16 v[60:63], v[168:171], v[208:211], v[60:63]
	v_mfma_f32_16x16x32_bf16 v[56:59], v[176:179], v[208:211], v[56:59]
	s_barrier
	v_mfma_f32_16x16x32_bf16 v[52:55], v[168:171], v[216:219], v[52:55]
	v_mfma_f32_16x16x32_bf16 v[48:51], v[176:179], v[216:219], v[48:51]
	v_mfma_f32_16x16x32_bf16 v[44:47], v[168:171], v[224:227], v[44:47]
	v_mfma_f32_16x16x32_bf16 v[40:43], v[176:179], v[224:227], v[40:43]
	v_mfma_f32_16x16x32_bf16 v[72:75], v[172:175], v[204:207], v[72:75]
	v_mfma_f32_16x16x32_bf16 v[64:67], v[180:183], v[204:207], v[64:67]
	v_mfma_f32_16x16x32_bf16 v[60:63], v[172:175], v[212:215], v[60:63]
	v_mfma_f32_16x16x32_bf16 v[56:59], v[180:183], v[212:215], v[56:59]
	v_mfma_f32_16x16x32_bf16 v[52:55], v[172:175], v[220:223], v[52:55]
	v_mfma_f32_16x16x32_bf16 v[48:51], v[180:183], v[220:223], v[48:51]
	v_mfma_f32_16x16x32_bf16 v[44:47], v[172:175], v[228:231], v[44:47]
	v_mfma_f32_16x16x32_bf16 v[40:43], v[180:183], v[228:231], v[40:43]
	s_setprio 0
	s_setprio 1
	v_mfma_f32_16x16x32_bf16 v[36:39], v[184:187], v[200:203], v[36:39]
	v_mfma_f32_16x16x32_bf16 v[32:35], v[192:195], v[200:203], v[32:35]
	v_mfma_f32_16x16x32_bf16 v[28:31], v[184:187], v[208:211], v[28:31]
	v_mfma_f32_16x16x32_bf16 v[24:27], v[192:195], v[208:211], v[24:27]
	v_mfma_f32_16x16x32_bf16 v[20:23], v[184:187], v[216:219], v[20:23]
	v_mfma_f32_16x16x32_bf16 v[16:19], v[192:195], v[216:219], v[16:19]
	v_mfma_f32_16x16x32_bf16 v[12:15], v[184:187], v[224:227], v[12:15]
	v_mfma_f32_16x16x32_bf16 v[8:11], v[192:195], v[224:227], v[8:11]
	v_mfma_f32_16x16x32_bf16 v[36:39], v[188:191], v[204:207], v[36:39]
	v_mfma_f32_16x16x32_bf16 v[32:35], v[196:199], v[204:207], v[32:35]
	v_mfma_f32_16x16x32_bf16 v[28:31], v[188:191], v[212:215], v[28:31]
	v_mfma_f32_16x16x32_bf16 v[24:27], v[196:199], v[212:215], v[24:27]
	v_mfma_f32_16x16x32_bf16 v[20:23], v[188:191], v[220:223], v[20:23]
	v_mfma_f32_16x16x32_bf16 v[16:19], v[196:199], v[220:223], v[16:19]
	v_mfma_f32_16x16x32_bf16 v[12:15], v[188:191], v[228:231], v[12:15]
	v_mfma_f32_16x16x32_bf16 v[8:11], v[196:199], v[228:231], v[8:11]
	s_setprio 0
	s_barrier
	s_add_i32 s45, s67, s41
	v_lshl_add_u64 v[234:235], v[232:233], 0, v[138:139]
	s_mov_b32 m0, s45
	ds_read_b128 v[200:203], v160 offset:16384
	ds_read_b128 v[204:207], v160 offset:17408
	ds_read_b128 v[208:211], v160 offset:18432
	ds_read_b128 v[212:215], v160 offset:19456
	ds_read_b128 v[216:219], v160 offset:20480
	ds_read_b128 v[220:223], v160 offset:21504
	ds_read_b128 v[224:227], v160 offset:22528
	ds_read_b128 v[228:231], v160 offset:23552
	global_load_lds_dwordx4 v[234:235], off
	v_lshl_add_u64 v[236:237], v[232:233], 0, v[140:141]
	s_add_i32 m0, s45, 0x2000
	v_lshl_add_u64 v[238:239], v[232:233], 0, s[12:13]
	s_add_i32 s45, s68, s41
	global_load_lds_dwordx4 v[236:237], off
	v_lshl_add_u64 v[240:241], v[238:239], 0, v[138:139]
	s_mov_b32 m0, s45
	v_lshl_add_u64 v[238:239], v[238:239], 0, v[140:141]
	global_load_lds_dwordx4 v[240:241], off
	s_add_i32 m0, s45, 0x2000
	v_cndmask_b32_e32 v130, v162, v165, vcc
	global_load_lds_dwordx4 v[238:239], off
	s_mov_b32 m0, s42
	v_cndmask_b32_e32 v238, v136, v164, vcc
	global_load_lds_dwordx4 v130, s[38:39]
	s_mov_b32 m0, s43
	v_mov_b32_e32 v239, v131
	global_load_lds_dwordx4 v238, s[38:39]
	s_waitcnt vmcnt(8)
	s_waitcnt lgkmcnt(0)
	v_lshl_add_u64 v[240:241], s[38:39], 0, v[130:131]
	v_lshl_add_u64 v[238:239], s[38:39], 0, v[238:239]
	s_setprio 1
	s_waitcnt lgkmcnt(0)
	v_mfma_f32_16x16x32_bf16 v[4:7], v[168:171], v[200:203], v[4:7]
	v_mfma_f32_16x16x32_bf16 v[0:3], v[176:179], v[200:203], v[0:3]
	v_mfma_f32_16x16x32_bf16 v[68:71], v[168:171], v[208:211], v[68:71]
	v_mfma_f32_16x16x32_bf16 v[76:79], v[176:179], v[208:211], v[76:79]
	s_barrier
	v_mfma_f32_16x16x32_bf16 v[80:83], v[168:171], v[216:219], v[80:83]
	v_mfma_f32_16x16x32_bf16 v[84:87], v[176:179], v[216:219], v[84:87]
	v_mfma_f32_16x16x32_bf16 v[88:91], v[168:171], v[224:227], v[88:91]
	v_mfma_f32_16x16x32_bf16 v[92:95], v[176:179], v[224:227], v[92:95]
	v_mfma_f32_16x16x32_bf16 v[4:7], v[172:175], v[204:207], v[4:7]
	v_mfma_f32_16x16x32_bf16 v[0:3], v[180:183], v[204:207], v[0:3]
	v_mfma_f32_16x16x32_bf16 v[68:71], v[172:175], v[212:215], v[68:71]
	v_mfma_f32_16x16x32_bf16 v[76:79], v[180:183], v[212:215], v[76:79]
	v_mfma_f32_16x16x32_bf16 v[80:83], v[172:175], v[220:223], v[80:83]
	v_mfma_f32_16x16x32_bf16 v[84:87], v[180:183], v[220:223], v[84:87]
	v_mfma_f32_16x16x32_bf16 v[88:91], v[172:175], v[228:231], v[88:91]
	v_mfma_f32_16x16x32_bf16 v[92:95], v[180:183], v[228:231], v[92:95]
	s_setprio 0
	s_setprio 1
	v_mfma_f32_16x16x32_bf16 v[96:99], v[184:187], v[200:203], v[96:99]
	v_mfma_f32_16x16x32_bf16 v[100:103], v[192:195], v[200:203], v[100:103]
	v_mfma_f32_16x16x32_bf16 v[104:107], v[184:187], v[208:211], v[104:107]
	v_mfma_f32_16x16x32_bf16 v[108:111], v[192:195], v[208:211], v[108:111]
	v_mfma_f32_16x16x32_bf16 v[112:115], v[184:187], v[216:219], v[112:115]
	v_mfma_f32_16x16x32_bf16 v[116:119], v[192:195], v[216:219], v[116:119]
	v_mfma_f32_16x16x32_bf16 v[120:123], v[184:187], v[224:227], v[120:123]
	v_mfma_f32_16x16x32_bf16 v[124:127], v[192:195], v[224:227], v[124:127]
	v_mfma_f32_16x16x32_bf16 v[96:99], v[188:191], v[204:207], v[96:99]
	v_mfma_f32_16x16x32_bf16 v[100:103], v[196:199], v[204:207], v[100:103]
	v_mfma_f32_16x16x32_bf16 v[104:107], v[188:191], v[212:215], v[104:107]
	v_mfma_f32_16x16x32_bf16 v[108:111], v[196:199], v[212:215], v[108:111]
	v_mfma_f32_16x16x32_bf16 v[112:115], v[188:191], v[220:223], v[112:115]
	v_mfma_f32_16x16x32_bf16 v[116:119], v[196:199], v[220:223], v[116:119]
	v_mfma_f32_16x16x32_bf16 v[120:123], v[188:191], v[228:231], v[120:123]
	v_mfma_f32_16x16x32_bf16 v[124:127], v[196:199], v[228:231], v[124:127]
	s_setprio 0
	s_barrier
	s_add_i32 s45, 0, 0x18000
	v_add_u32_e32 v130, s45, v159
	s_add_i32 s46, 0, 0x1c000
	ds_read_b128 v[168:171], v130
	ds_read_b128 v[172:175], v130 offset:1024
	ds_read_b128 v[176:179], v130 offset:2048
	ds_read_b128 v[180:183], v130 offset:3072
	v_add_u32_e32 v130, s46, v159
	ds_read_b128 v[184:187], v130
	ds_read_b128 v[188:191], v130 offset:1024
	ds_read_b128 v[192:195], v130 offset:2048
	ds_read_b128 v[196:199], v130 offset:3072
	s_mov_b32 m0, s48
	v_cndmask_b32_e32 v130, v134, v161, vcc
	ds_read_b128 v[200:203], v160 offset:32768
	ds_read_b128 v[204:207], v160 offset:33792
	ds_read_b128 v[208:211], v160 offset:34816
	ds_read_b128 v[212:215], v160 offset:35840
	ds_read_b128 v[216:219], v160 offset:36864
	ds_read_b128 v[220:223], v160 offset:37888
	ds_read_b128 v[224:227], v160 offset:38912
	ds_read_b128 v[228:231], v160 offset:39936
	v_cndmask_b32_e32 v133, v132, v163, vcc
	global_load_lds_dwordx4 v130, s[38:39]
	s_mov_b32 m0, s49
	s_nop 0
	global_load_lds_dwordx4 v133, s[38:39]
	s_waitcnt vmcnt(8)
	s_waitcnt lgkmcnt(0)
	s_setprio 1
	s_waitcnt lgkmcnt(0)
	v_mfma_f32_16x16x32_bf16 v[72:75], v[168:171], v[200:203], v[72:75]
	v_mfma_f32_16x16x32_bf16 v[64:67], v[176:179], v[200:203], v[64:67]
	v_mfma_f32_16x16x32_bf16 v[60:63], v[168:171], v[208:211], v[60:63]
	v_mfma_f32_16x16x32_bf16 v[56:59], v[176:179], v[208:211], v[56:59]
	s_barrier
	v_mfma_f32_16x16x32_bf16 v[52:55], v[168:171], v[216:219], v[52:55]
	v_mfma_f32_16x16x32_bf16 v[48:51], v[176:179], v[216:219], v[48:51]
	v_mfma_f32_16x16x32_bf16 v[44:47], v[168:171], v[224:227], v[44:47]
	v_mfma_f32_16x16x32_bf16 v[40:43], v[176:179], v[224:227], v[40:43]
	v_mfma_f32_16x16x32_bf16 v[72:75], v[172:175], v[204:207], v[72:75]
	v_mfma_f32_16x16x32_bf16 v[64:67], v[180:183], v[204:207], v[64:67]
	v_mfma_f32_16x16x32_bf16 v[60:63], v[172:175], v[212:215], v[60:63]
	v_mfma_f32_16x16x32_bf16 v[56:59], v[180:183], v[212:215], v[56:59]
	v_mfma_f32_16x16x32_bf16 v[52:55], v[172:175], v[220:223], v[52:55]
	v_mfma_f32_16x16x32_bf16 v[48:51], v[180:183], v[220:223], v[48:51]
	v_mfma_f32_16x16x32_bf16 v[44:47], v[172:175], v[228:231], v[44:47]
	v_mfma_f32_16x16x32_bf16 v[40:43], v[180:183], v[228:231], v[40:43]
	s_setprio 0
	s_setprio 1
	v_mfma_f32_16x16x32_bf16 v[36:39], v[184:187], v[200:203], v[36:39]
	v_mfma_f32_16x16x32_bf16 v[32:35], v[192:195], v[200:203], v[32:35]
	v_mfma_f32_16x16x32_bf16 v[28:31], v[184:187], v[208:211], v[28:31]
	v_mfma_f32_16x16x32_bf16 v[24:27], v[192:195], v[208:211], v[24:27]
	v_mfma_f32_16x16x32_bf16 v[20:23], v[184:187], v[216:219], v[20:23]
	v_mfma_f32_16x16x32_bf16 v[16:19], v[192:195], v[216:219], v[16:19]
	v_mfma_f32_16x16x32_bf16 v[12:15], v[184:187], v[224:227], v[12:15]
	v_mfma_f32_16x16x32_bf16 v[8:11], v[192:195], v[224:227], v[8:11]
	v_mfma_f32_16x16x32_bf16 v[36:39], v[188:191], v[204:207], v[36:39]
	v_mfma_f32_16x16x32_bf16 v[32:35], v[196:199], v[204:207], v[32:35]
	v_mfma_f32_16x16x32_bf16 v[28:31], v[188:191], v[212:215], v[28:31]
	v_mfma_f32_16x16x32_bf16 v[24:27], v[196:199], v[212:215], v[24:27]
	v_mfma_f32_16x16x32_bf16 v[20:23], v[188:191], v[220:223], v[20:23]
	v_mfma_f32_16x16x32_bf16 v[16:19], v[196:199], v[220:223], v[16:19]
	v_mfma_f32_16x16x32_bf16 v[12:15], v[188:191], v[228:231], v[12:15]
	v_mfma_f32_16x16x32_bf16 v[8:11], v[196:199], v[228:231], v[8:11]
	s_setprio 0
	s_barrier
	s_add_i32 s38, s45, s41
	v_lshl_add_u64 v[234:235], v[234:235], 0, s[20:21]
	s_mov_b32 m0, s38
	ds_read_b128 v[200:203], v160 offset:49152
	ds_read_b128 v[204:207], v160 offset:50176
	ds_read_b128 v[208:211], v160 offset:51200
	ds_read_b128 v[212:215], v160 offset:52224
	ds_read_b128 v[216:219], v160 offset:53248
	ds_read_b128 v[220:223], v160 offset:54272
	ds_read_b128 v[224:227], v160 offset:55296
	ds_read_b128 v[228:231], v160 offset:56320
	global_load_lds_dwordx4 v[234:235], off
	v_lshl_add_u64 v[234:235], v[236:237], 0, s[20:21]
	s_add_i32 m0, s38, 0x2000
	v_lshl_add_u64 v[232:233], v[232:233], 0, s[24:25]
	s_add_i32 s38, s46, s41
	global_load_lds_dwordx4 v[234:235], off
	v_lshl_add_u64 v[234:235], v[232:233], 0, v[138:139]
	s_mov_b32 m0, s38
	v_lshl_add_u64 v[232:233], v[232:233], 0, v[140:141]
	global_load_lds_dwordx4 v[234:235], off
	s_add_i32 m0, s38, 0x2000
	s_nop 0
	global_load_lds_dwordx4 v[232:233], off
	v_lshl_add_u64 v[232:233], v[240:241], 0, s[20:21]
	s_mov_b32 m0, s52
	s_nop 0
	global_load_lds_dwordx4 v[232:233], off
	v_lshl_add_u64 v[232:233], v[238:239], 0, s[20:21]
	s_mov_b32 m0, s53
	s_nop 0
	global_load_lds_dwordx4 v[232:233], off
	s_waitcnt vmcnt(8)
	s_waitcnt lgkmcnt(0)
	s_setprio 1
	s_waitcnt lgkmcnt(0)
	v_mfma_f32_16x16x32_bf16 v[4:7], v[168:171], v[200:203], v[4:7]
	v_mfma_f32_16x16x32_bf16 v[0:3], v[176:179], v[200:203], v[0:3]
	v_mfma_f32_16x16x32_bf16 v[68:71], v[168:171], v[208:211], v[68:71]
	v_mfma_f32_16x16x32_bf16 v[76:79], v[176:179], v[208:211], v[76:79]
	s_barrier
	v_mfma_f32_16x16x32_bf16 v[80:83], v[168:171], v[216:219], v[80:83]
	v_mfma_f32_16x16x32_bf16 v[84:87], v[176:179], v[216:219], v[84:87]
	v_mfma_f32_16x16x32_bf16 v[88:91], v[168:171], v[224:227], v[88:91]
	v_mfma_f32_16x16x32_bf16 v[92:95], v[176:179], v[224:227], v[92:95]
	v_mfma_f32_16x16x32_bf16 v[4:7], v[172:175], v[204:207], v[4:7]
	v_mfma_f32_16x16x32_bf16 v[0:3], v[180:183], v[204:207], v[0:3]
	v_mfma_f32_16x16x32_bf16 v[68:71], v[172:175], v[212:215], v[68:71]
	v_mfma_f32_16x16x32_bf16 v[76:79], v[180:183], v[212:215], v[76:79]
	v_mfma_f32_16x16x32_bf16 v[80:83], v[172:175], v[220:223], v[80:83]
	v_mfma_f32_16x16x32_bf16 v[84:87], v[180:183], v[220:223], v[84:87]
	v_mfma_f32_16x16x32_bf16 v[88:91], v[172:175], v[228:231], v[88:91]
	v_mfma_f32_16x16x32_bf16 v[92:95], v[180:183], v[228:231], v[92:95]
	s_setprio 0
	s_setprio 1
	v_mfma_f32_16x16x32_bf16 v[96:99], v[184:187], v[200:203], v[96:99]
	v_mfma_f32_16x16x32_bf16 v[100:103], v[192:195], v[200:203], v[100:103]
	v_mfma_f32_16x16x32_bf16 v[104:107], v[184:187], v[208:211], v[104:107]
	v_mfma_f32_16x16x32_bf16 v[108:111], v[192:195], v[208:211], v[108:111]
	v_mfma_f32_16x16x32_bf16 v[112:115], v[184:187], v[216:219], v[112:115]
	v_mfma_f32_16x16x32_bf16 v[116:119], v[192:195], v[216:219], v[116:119]
	v_mfma_f32_16x16x32_bf16 v[120:123], v[184:187], v[224:227], v[120:123]
	v_mfma_f32_16x16x32_bf16 v[124:127], v[192:195], v[224:227], v[124:127]
	v_mfma_f32_16x16x32_bf16 v[96:99], v[188:191], v[204:207], v[96:99]
	v_mfma_f32_16x16x32_bf16 v[100:103], v[196:199], v[204:207], v[100:103]
	v_mfma_f32_16x16x32_bf16 v[104:107], v[188:191], v[212:215], v[104:107]
	v_mfma_f32_16x16x32_bf16 v[108:111], v[196:199], v[212:215], v[108:111]
	v_mfma_f32_16x16x32_bf16 v[112:115], v[188:191], v[220:223], v[112:115]
	v_mfma_f32_16x16x32_bf16 v[116:119], v[196:199], v[220:223], v[116:119]
	v_mfma_f32_16x16x32_bf16 v[120:123], v[188:191], v[228:231], v[120:123]
	v_mfma_f32_16x16x32_bf16 v[124:127], v[196:199], v[228:231], v[124:127]
	s_setprio 0
	s_barrier
	s_add_i32 s44, s44, 2
	s_add_u32 s36, s36, 0x100
	s_addc_u32 s37, s37, 0
	s_cmp_gt_u32 s44, 29
	s_cbranch_scc0 .LBB0_1576
	s_and_b64 vcc, exec, s[26:27]
	s_cbranch_vccz .LBB0_1579
	s_barrier

.LBB0_1714:
	v_add_u32_e32 v161, s56, v157
	ds_read_b128 v[162:165], v161
	ds_read_b128 v[166:169], v161 offset:1024
	ds_read_b128 v[170:173], v161 offset:2048
	ds_read_b128 v[174:177], v161 offset:3072
	v_add_u32_e32 v161, s57, v157
	ds_read_b128 v[178:181], v161
	ds_read_b128 v[182:185], v161 offset:1024
	ds_read_b128 v[186:189], v161 offset:2048
	ds_read_b128 v[190:193], v161 offset:3072
	s_cmp_eq_u32 s36, 4
	v_lshl_add_u64 v[194:195], v[152:153], 0, s[22:23]
	s_cselect_b64 vcc, -1, 0
	v_cndmask_b32_e32 v227, v195, v143, vcc
	v_cndmask_b32_e32 v226, v194, v147, vcc
	v_cndmask_b32_e32 v229, v155, v145, vcc
	v_cndmask_b32_e32 v228, v154, v160, vcc
	v_lshl_add_u64 v[230:231], v[152:153], 0, v[138:139]
	s_add_i32 m0, s39, 0xc000
	ds_read_b128 v[194:197], v159
	ds_read_b128 v[198:201], v159 offset:1024
	ds_read_b128 v[202:205], v159 offset:2048
	ds_read_b128 v[206:209], v159 offset:3072
	ds_read_b128 v[210:213], v159 offset:4096
	ds_read_b128 v[214:217], v159 offset:5120
	ds_read_b128 v[218:221], v159 offset:6144
	ds_read_b128 v[222:225], v159 offset:7168
	global_load_lds_dwordx4 v[230:231], off
	v_lshl_add_u64 v[230:231], v[152:153], 0, v[140:141]
	s_add_i32 m0, s39, 0xe000
	s_nop 0
	global_load_lds_dwordx4 v[230:231], off
	s_waitcnt vmcnt(8)
	s_waitcnt lgkmcnt(0)
	s_setprio 1
	s_waitcnt lgkmcnt(0)
	v_mfma_f32_16x16x32_bf16 v[124:127], v[162:165], v[194:197], v[124:127]
	v_mfma_f32_16x16x32_bf16 v[120:123], v[170:173], v[194:197], v[120:123]
	v_mfma_f32_16x16x32_bf16 v[116:119], v[162:165], v[202:205], v[116:119]
	v_mfma_f32_16x16x32_bf16 v[108:111], v[170:173], v[202:205], v[108:111]
	s_barrier
	v_mfma_f32_16x16x32_bf16 v[100:103], v[162:165], v[210:213], v[100:103]
	v_mfma_f32_16x16x32_bf16 v[92:95], v[170:173], v[210:213], v[92:95]
	v_mfma_f32_16x16x32_bf16 v[80:83], v[162:165], v[218:221], v[80:83]
	v_mfma_f32_16x16x32_bf16 v[72:75], v[170:173], v[218:221], v[72:75]
	v_mfma_f32_16x16x32_bf16 v[124:127], v[166:169], v[198:201], v[124:127]
	v_mfma_f32_16x16x32_bf16 v[120:123], v[174:177], v[198:201], v[120:123]
	v_mfma_f32_16x16x32_bf16 v[116:119], v[166:169], v[206:209], v[116:119]
	v_mfma_f32_16x16x32_bf16 v[108:111], v[174:177], v[206:209], v[108:111]
	v_mfma_f32_16x16x32_bf16 v[100:103], v[166:169], v[214:217], v[100:103]
	v_mfma_f32_16x16x32_bf16 v[92:95], v[174:177], v[214:217], v[92:95]
	v_mfma_f32_16x16x32_bf16 v[80:83], v[166:169], v[222:225], v[80:83]
	v_mfma_f32_16x16x32_bf16 v[72:75], v[174:177], v[222:225], v[72:75]
	s_setprio 0
	s_setprio 1
	v_mfma_f32_16x16x32_bf16 v[112:115], v[178:181], v[194:197], v[112:115]
	v_mfma_f32_16x16x32_bf16 v[104:107], v[186:189], v[194:197], v[104:107]
	v_mfma_f32_16x16x32_bf16 v[96:99], v[178:181], v[202:205], v[96:99]
	v_mfma_f32_16x16x32_bf16 v[88:91], v[186:189], v[202:205], v[88:91]
	v_mfma_f32_16x16x32_bf16 v[84:87], v[178:181], v[210:213], v[84:87]
	v_mfma_f32_16x16x32_bf16 v[76:79], v[186:189], v[210:213], v[76:79]
	v_mfma_f32_16x16x32_bf16 v[68:71], v[178:181], v[218:221], v[68:71]
	v_mfma_f32_16x16x32_bf16 v[64:67], v[186:189], v[218:221], v[64:67]
	v_mfma_f32_16x16x32_bf16 v[112:115], v[182:185], v[198:201], v[112:115]
	v_mfma_f32_16x16x32_bf16 v[104:107], v[190:193], v[198:201], v[104:107]
	v_mfma_f32_16x16x32_bf16 v[96:99], v[182:185], v[206:209], v[96:99]
	v_mfma_f32_16x16x32_bf16 v[88:91], v[190:193], v[206:209], v[88:91]
	v_mfma_f32_16x16x32_bf16 v[84:87], v[182:185], v[214:217], v[84:87]
	v_mfma_f32_16x16x32_bf16 v[76:79], v[190:193], v[214:217], v[76:79]
	v_mfma_f32_16x16x32_bf16 v[68:71], v[182:185], v[222:225], v[68:71]
	v_mfma_f32_16x16x32_bf16 v[64:67], v[190:193], v[222:225], v[64:67]
	s_setprio 0
	s_barrier
	s_add_i32 s37, s56, s38
	v_lshl_add_u64 v[230:231], v[228:229], 0, v[130:131]
	s_mov_b32 m0, s37
	ds_read_b128 v[194:197], v159 offset:16384
	ds_read_b128 v[198:201], v159 offset:17408
	ds_read_b128 v[202:205], v159 offset:18432
	ds_read_b128 v[206:209], v159 offset:19456
	ds_read_b128 v[210:213], v159 offset:20480
	ds_read_b128 v[214:217], v159 offset:21504
	ds_read_b128 v[218:221], v159 offset:22528
	ds_read_b128 v[222:225], v159 offset:23552
	global_load_lds_dwordx4 v[230:231], off
	v_lshl_add_u64 v[232:233], v[228:229], 0, v[134:135]
	s_add_i32 m0, s37, 0x2000
	v_lshl_add_u64 v[234:235], v[228:229], 0, s[10:11]
	s_add_i32 s37, s57, s38
	global_load_lds_dwordx4 v[232:233], off
	v_lshl_add_u64 v[236:237], v[234:235], 0, v[130:131]
	s_mov_b32 m0, s37
	v_lshl_add_u64 v[234:235], v[234:235], 0, v[134:135]
	global_load_lds_dwordx4 v[236:237], off
	s_add_i32 m0, s37, 0x2000
	v_lshl_add_u64 v[236:237], v[226:227], 0, v[132:133]
	global_load_lds_dwordx4 v[234:235], off
	v_lshl_add_u64 v[234:235], v[226:227], 0, v[128:129]
	s_mov_b32 m0, s39
	s_nop 0
	global_load_lds_dwordx4 v[234:235], off
	s_mov_b32 m0, s40
	s_nop 0
	global_load_lds_dwordx4 v[236:237], off
	s_waitcnt vmcnt(8)
	s_waitcnt lgkmcnt(0)
	s_setprio 1
	s_waitcnt lgkmcnt(0)
	v_mfma_f32_16x16x32_bf16 v[60:63], v[162:165], v[194:197], v[60:63]
	v_mfma_f32_16x16x32_bf16 v[56:59], v[170:173], v[194:197], v[56:59]
	v_mfma_f32_16x16x32_bf16 v[52:55], v[162:165], v[202:205], v[52:55]
	v_mfma_f32_16x16x32_bf16 v[44:47], v[170:173], v[202:205], v[44:47]
	s_barrier
	v_mfma_f32_16x16x32_bf16 v[36:39], v[162:165], v[210:213], v[36:39]
	v_mfma_f32_16x16x32_bf16 v[28:31], v[170:173], v[210:213], v[28:31]
	v_mfma_f32_16x16x32_bf16 v[20:23], v[162:165], v[218:221], v[20:23]
	v_mfma_f32_16x16x32_bf16 v[12:15], v[170:173], v[218:221], v[12:15]
	v_mfma_f32_16x16x32_bf16 v[60:63], v[166:169], v[198:201], v[60:63]
	v_mfma_f32_16x16x32_bf16 v[56:59], v[174:177], v[198:201], v[56:59]
	v_mfma_f32_16x16x32_bf16 v[52:55], v[166:169], v[206:209], v[52:55]
	v_mfma_f32_16x16x32_bf16 v[44:47], v[174:177], v[206:209], v[44:47]
	v_mfma_f32_16x16x32_bf16 v[36:39], v[166:169], v[214:217], v[36:39]
	v_mfma_f32_16x16x32_bf16 v[28:31], v[174:177], v[214:217], v[28:31]
	v_mfma_f32_16x16x32_bf16 v[20:23], v[166:169], v[222:225], v[20:23]
	v_mfma_f32_16x16x32_bf16 v[12:15], v[174:177], v[222:225], v[12:15]
	s_setprio 0
	s_setprio 1
	v_mfma_f32_16x16x32_bf16 v[48:51], v[178:181], v[194:197], v[48:51]
	v_mfma_f32_16x16x32_bf16 v[40:43], v[186:189], v[194:197], v[40:43]
	v_mfma_f32_16x16x32_bf16 v[32:35], v[178:181], v[202:205], v[32:35]
	v_mfma_f32_16x16x32_bf16 v[24:27], v[186:189], v[202:205], v[24:27]
	v_mfma_f32_16x16x32_bf16 v[16:19], v[178:181], v[210:213], v[16:19]
	v_mfma_f32_16x16x32_bf16 v[8:11], v[186:189], v[210:213], v[8:11]
	v_mfma_f32_16x16x32_bf16 v[4:7], v[178:181], v[218:221], v[4:7]
	v_mfma_f32_16x16x32_bf16 v[0:3], v[186:189], v[218:221], v[0:3]
	v_mfma_f32_16x16x32_bf16 v[48:51], v[182:185], v[198:201], v[48:51]
	v_mfma_f32_16x16x32_bf16 v[40:43], v[190:193], v[198:201], v[40:43]
	v_mfma_f32_16x16x32_bf16 v[32:35], v[182:185], v[206:209], v[32:35]
	v_mfma_f32_16x16x32_bf16 v[24:27], v[190:193], v[206:209], v[24:27]
	v_mfma_f32_16x16x32_bf16 v[16:19], v[182:185], v[214:217], v[16:19]
	v_mfma_f32_16x16x32_bf16 v[8:11], v[190:193], v[214:217], v[8:11]
	v_mfma_f32_16x16x32_bf16 v[4:7], v[182:185], v[222:225], v[4:7]
	v_mfma_f32_16x16x32_bf16 v[0:3], v[190:193], v[222:225], v[0:3]
	s_setprio 0
	s_barrier
	s_add_i32 s37, 0, 0x18000
	v_add_u32_e32 v161, s37, v157
	s_add_i32 s62, 0, 0x1c000
	ds_read_b128 v[162:165], v161
	ds_read_b128 v[166:169], v161 offset:1024
	ds_read_b128 v[170:173], v161 offset:2048
	ds_read_b128 v[174:177], v161 offset:3072
	v_add_u32_e32 v161, s62, v157
	ds_read_b128 v[178:181], v161
	ds_read_b128 v[182:185], v161 offset:1024
	ds_read_b128 v[186:189], v161 offset:2048
	ds_read_b128 v[190:193], v161 offset:3072
	v_lshl_add_u64 v[226:227], v[226:227], 0, s[10:11]
	s_mov_b32 m0, s41
	v_lshl_add_u64 v[238:239], v[226:227], 0, v[128:129]
	ds_read_b128 v[194:197], v159 offset:32768
	ds_read_b128 v[198:201], v159 offset:33792
	ds_read_b128 v[202:205], v159 offset:34816
	ds_read_b128 v[206:209], v159 offset:35840
	ds_read_b128 v[210:213], v159 offset:36864
	ds_read_b128 v[214:217], v159 offset:37888
	ds_read_b128 v[218:221], v159 offset:38912
	ds_read_b128 v[222:225], v159 offset:39936
	global_load_lds_dwordx4 v[238:239], off
	v_lshl_add_u64 v[226:227], v[226:227], 0, v[132:133]
	s_mov_b32 m0, s42
	s_nop 0
	global_load_lds_dwordx4 v[226:227], off
	s_waitcnt vmcnt(8)
	s_waitcnt lgkmcnt(0)
	s_setprio 1
	s_waitcnt lgkmcnt(0)
	v_mfma_f32_16x16x32_bf16 v[124:127], v[162:165], v[194:197], v[124:127]
	v_mfma_f32_16x16x32_bf16 v[120:123], v[170:173], v[194:197], v[120:123]
	v_mfma_f32_16x16x32_bf16 v[116:119], v[162:165], v[202:205], v[116:119]
	v_mfma_f32_16x16x32_bf16 v[108:111], v[170:173], v[202:205], v[108:111]
	s_barrier
	v_mfma_f32_16x16x32_bf16 v[100:103], v[162:165], v[210:213], v[100:103]
	v_mfma_f32_16x16x32_bf16 v[92:95], v[170:173], v[210:213], v[92:95]
	v_mfma_f32_16x16x32_bf16 v[80:83], v[162:165], v[218:221], v[80:83]
	v_mfma_f32_16x16x32_bf16 v[72:75], v[170:173], v[218:221], v[72:75]
	v_mfma_f32_16x16x32_bf16 v[124:127], v[166:169], v[198:201], v[124:127]
	v_mfma_f32_16x16x32_bf16 v[120:123], v[174:177], v[198:201], v[120:123]
	v_mfma_f32_16x16x32_bf16 v[116:119], v[166:169], v[206:209], v[116:119]
	v_mfma_f32_16x16x32_bf16 v[108:111], v[174:177], v[206:209], v[108:111]
	v_mfma_f32_16x16x32_bf16 v[100:103], v[166:169], v[214:217], v[100:103]
	v_mfma_f32_16x16x32_bf16 v[92:95], v[174:177], v[214:217], v[92:95]
	v_mfma_f32_16x16x32_bf16 v[80:83], v[166:169], v[222:225], v[80:83]
	v_mfma_f32_16x16x32_bf16 v[72:75], v[174:177], v[222:225], v[72:75]
	s_setprio 0
	s_setprio 1
	v_mfma_f32_16x16x32_bf16 v[112:115], v[178:181], v[194:197], v[112:115]
	v_mfma_f32_16x16x32_bf16 v[104:107], v[186:189], v[194:197], v[104:107]
	v_mfma_f32_16x16x32_bf16 v[96:99], v[178:181], v[202:205], v[96:99]
	v_mfma_f32_16x16x32_bf16 v[88:91], v[186:189], v[202:205], v[88:91]
	v_mfma_f32_16x16x32_bf16 v[84:87], v[178:181], v[210:213], v[84:87]
	v_mfma_f32_16x16x32_bf16 v[76:79], v[186:189], v[210:213], v[76:79]
	v_mfma_f32_16x16x32_bf16 v[68:71], v[178:181], v[218:221], v[68:71]
	v_mfma_f32_16x16x32_bf16 v[64:67], v[186:189], v[218:221], v[64:67]
	v_mfma_f32_16x16x32_bf16 v[112:115], v[182:185], v[198:201], v[112:115]
	v_mfma_f32_16x16x32_bf16 v[104:107], v[190:193], v[198:201], v[104:107]
	v_mfma_f32_16x16x32_bf16 v[96:99], v[182:185], v[206:209], v[96:99]
	v_mfma_f32_16x16x32_bf16 v[88:91], v[190:193], v[206:209], v[88:91]
	v_mfma_f32_16x16x32_bf16 v[84:87], v[182:185], v[214:217], v[84:87]
	v_mfma_f32_16x16x32_bf16 v[76:79], v[190:193], v[214:217], v[76:79]
	v_mfma_f32_16x16x32_bf16 v[68:71], v[182:185], v[222:225], v[68:71]
	v_mfma_f32_16x16x32_bf16 v[64:67], v[190:193], v[222:225], v[64:67]
	s_setprio 0
	s_barrier
	s_add_i32 s37, s37, s38
	v_lshl_add_u64 v[226:227], v[230:231], 0, s[14:15]
	s_mov_b32 m0, s37
	ds_read_b128 v[194:197], v159 offset:49152
	ds_read_b128 v[198:201], v159 offset:50176
	ds_read_b128 v[202:205], v159 offset:51200
	ds_read_b128 v[206:209], v159 offset:52224
	ds_read_b128 v[210:213], v159 offset:53248
	ds_read_b128 v[214:217], v159 offset:54272
	ds_read_b128 v[218:221], v159 offset:55296
	ds_read_b128 v[222:225], v159 offset:56320
	global_load_lds_dwordx4 v[226:227], off
	v_lshl_add_u64 v[226:227], v[232:233], 0, s[14:15]
	s_add_i32 m0, s37, 0x2000
	s_add_i32 s37, s62, s38
	global_load_lds_dwordx4 v[226:227], off
	v_lshl_add_u64 v[226:227], v[228:229], 0, s[16:17]
	v_lshl_add_u64 v[228:229], v[226:227], 0, v[130:131]
	s_mov_b32 m0, s37
	v_lshl_add_u64 v[226:227], v[226:227], 0, v[134:135]
	global_load_lds_dwordx4 v[228:229], off
	s_add_i32 m0, s37, 0x2000
	s_nop 0
	global_load_lds_dwordx4 v[226:227], off
	v_lshl_add_u64 v[226:227], v[234:235], 0, s[14:15]
	s_mov_b32 m0, s44
	s_nop 0
	global_load_lds_dwordx4 v[226:227], off
	v_lshl_add_u64 v[226:227], v[236:237], 0, s[14:15]
	s_mov_b32 m0, s45
	s_nop 0
	global_load_lds_dwordx4 v[226:227], off
	s_waitcnt vmcnt(8)
	s_waitcnt lgkmcnt(0)
	s_setprio 1
	s_waitcnt lgkmcnt(0)
	v_mfma_f32_16x16x32_bf16 v[60:63], v[162:165], v[194:197], v[60:63]
	v_mfma_f32_16x16x32_bf16 v[56:59], v[170:173], v[194:197], v[56:59]
	v_mfma_f32_16x16x32_bf16 v[52:55], v[162:165], v[202:205], v[52:55]
	v_mfma_f32_16x16x32_bf16 v[44:47], v[170:173], v[202:205], v[44:47]
	s_barrier
	v_mfma_f32_16x16x32_bf16 v[36:39], v[162:165], v[210:213], v[36:39]
	v_mfma_f32_16x16x32_bf16 v[28:31], v[170:173], v[210:213], v[28:31]
	v_mfma_f32_16x16x32_bf16 v[20:23], v[162:165], v[218:221], v[20:23]
	v_mfma_f32_16x16x32_bf16 v[12:15], v[170:173], v[218:221], v[12:15]
	v_mfma_f32_16x16x32_bf16 v[60:63], v[166:169], v[198:201], v[60:63]
	v_mfma_f32_16x16x32_bf16 v[56:59], v[174:177], v[198:201], v[56:59]
	v_mfma_f32_16x16x32_bf16 v[52:55], v[166:169], v[206:209], v[52:55]
	v_mfma_f32_16x16x32_bf16 v[44:47], v[174:177], v[206:209], v[44:47]
	v_mfma_f32_16x16x32_bf16 v[36:39], v[166:169], v[214:217], v[36:39]
	v_mfma_f32_16x16x32_bf16 v[28:31], v[174:177], v[214:217], v[28:31]
	v_mfma_f32_16x16x32_bf16 v[20:23], v[166:169], v[222:225], v[20:23]
	v_mfma_f32_16x16x32_bf16 v[12:15], v[174:177], v[222:225], v[12:15]
	s_setprio 0
	s_setprio 1
	v_mfma_f32_16x16x32_bf16 v[48:51], v[178:181], v[194:197], v[48:51]
	v_mfma_f32_16x16x32_bf16 v[40:43], v[186:189], v[194:197], v[40:43]
	v_mfma_f32_16x16x32_bf16 v[32:35], v[178:181], v[202:205], v[32:35]
	v_mfma_f32_16x16x32_bf16 v[24:27], v[186:189], v[202:205], v[24:27]
	v_mfma_f32_16x16x32_bf16 v[16:19], v[178:181], v[210:213], v[16:19]
	v_mfma_f32_16x16x32_bf16 v[8:11], v[186:189], v[210:213], v[8:11]
	v_mfma_f32_16x16x32_bf16 v[4:7], v[178:181], v[218:221], v[4:7]
	v_mfma_f32_16x16x32_bf16 v[0:3], v[186:189], v[218:221], v[0:3]
	v_mfma_f32_16x16x32_bf16 v[48:51], v[182:185], v[198:201], v[48:51]
	v_mfma_f32_16x16x32_bf16 v[40:43], v[190:193], v[198:201], v[40:43]
	v_mfma_f32_16x16x32_bf16 v[32:35], v[182:185], v[206:209], v[32:35]
	v_mfma_f32_16x16x32_bf16 v[24:27], v[190:193], v[206:209], v[24:27]
	v_mfma_f32_16x16x32_bf16 v[16:19], v[182:185], v[214:217], v[16:19]
	v_mfma_f32_16x16x32_bf16 v[8:11], v[190:193], v[214:217], v[8:11]
	v_mfma_f32_16x16x32_bf16 v[4:7], v[182:185], v[222:225], v[4:7]
	v_mfma_f32_16x16x32_bf16 v[0:3], v[190:193], v[222:225], v[0:3]
	s_setprio 0
	s_barrier
	s_add_i32 s36, s36, 2
	v_lshl_add_u64 v[152:153], v[152:153], 0, s[20:21]
	s_cmp_gt_u32 s36, 5
	v_lshl_add_u64 v[154:155], v[154:155], 0, s[20:21]
	s_cbranch_scc0 .LBB0_1714
	s_and_b64 vcc, exec, s[18:19]
	s_cbranch_vccz .LBB0_1717
	s_barrier
